# attention PV: V transposed reads re-addressed (lane bit5 <-> half offset) so the bf16 P operand needs no v_permlane32_swap: 8 fewer cross-lane ops per step
# speedup vs baseline: 1.0150x; 1.0150x over previous
; DI int tid_fresh(int wave) { return wave * 64 + lane_fresh(); }
; DI void attn_pass(const Frame& F, CvRide& cv, const bf16_t* __restrict__ Qb, const bf16_t* __restrict__ Kh, const bf16_t* __restrict__ Vh, char* lds, f32x16 (&o)[4], float& l_out, const int wave_s) {
;     const int tid = tid_fresh(wave_s), wid = tid >> 6, lane = tid & 63, r32 = lane & 31, hi = lane >> 5;
;     char* V_lds = lds + OFF_V; char* K_lds = lds + OFF_K;
;     float m_ref = 0.f, l_reg = 0.f; bf16x8 qr[4]; f32x16 negm = f32x16{};
; #pragma unroll
;     for (int d = 0; d < 4; ++d) o[d] = f32x16{};
;     const bf16_t* Qw = Qb + (size_t)(wid * 32 + r32) * 64 + hi * 8;
; #pragma unroll
;     for (int d0 = 0; d0 < 4; ++d0) qr[d0] = *reinterpret_cast<const bf16x8*>(Qw + d0 * 16);
;     const int sr = tid >> 4, sc = (tid & 15) * 8, vst0 = v_st(sr, sc), vst1 = v_st(32 + sr, sc);
;     const int kr = tid >> 3, kcb = (tid & 7) * 16, kst = AT_KSWZ(kr, kcb);
;     const int vb0 = (int)(uintptr_t)V_lds + v_rd_base(lane);
;     struct { bf16x8 vs0, vs1, ks0; } sr_[1];
;     const unsigned gvo = (unsigned)((sr * 128 + sc) * 2), gko = (unsigned)((kr * 64 + (tid & 7) * 8) * 2);
;     ...
;     const unsigned cv_ldo = (unsigned)(((tid >> 4) * 2 * 2048 + (tid & 15) * 4) * 4), cv_sto = (unsigned)((tid >> 3) * 2048 + 8 * (tid & 7));
;     const int cv_lw = OFF_CV + (4 * (tid & 15)) * 68 + 2 * (tid >> 4), cv_lr = OFF_CV + (tid >> 3) * 68 + 8 * (tid & 7);
;     f32x4 cvA = f32x4{}, cvB = f32x4{}; unsigned cvr0 = 0, cvr1 = 0;
;     ...
;     f32x16 pA0, pA1, pB0, pB1; float alA, alB; bf16x8 pa0, pa1, pa2, pa3; constexpr int NT = S / 64;
;     constexpr int SE = 0;
;     {
;         bf16x8 v10 = *reinterpret_cast<const bf16x8*>(&Vh[(size_t)(64 + sr) * 128 + sc]), v11 = *reinterpret_cast<const bf16x8*>(&Vh[(size_t)(96 + sr) * 128 + sc]);
;         bf16x8 k10 = *reinterpret_cast<const bf16x8*>(&Kh[(size_t)(64 + kr) * 64 + (tid & 7) * 8]);
;         AT_SLOAD(SE, 0); asm volatile("s_waitcnt vmcnt(0)" ::: "memory");
;         __syncthreads();
;         AT_SWRITE(0, SE);
;         *(bf16x8*)(V_lds + SHM_V + vst0) = v10; *(bf16x8*)(V_lds + SHM_V + vst1) = v11; *(bf16x8*)(K_lds + SHM_K + kst) = k10;
;         __syncthreads();
;     }
;     qkt(pA0, pA1, K_lds, qr, negm, r32, hi); partialSM(pA0, pA1, m_ref, negm, alA);
;     int s_prev = 0, s_cur = 1, s_next = 2;
.LBB4_691:
	v_lshlrev_b32_e32 v24, 4, v21
	v_lshlrev_b32_e32 v23, 3, v21
	v_and_b32_e32 v24, 0xc0, v24
	v_lshlrev_b32_e32 v21, 1, v21
	v_and_or_b32 v24, v23, 24, v24
	v_and_b32_e32 v21, 32, v21
	v_and_b32_e32 v23, 0x100, v23
	s_cmp_lg_u32 0, -1
	v_or3_b32 v199, v24, v21, v23
	s_cselect_b32 s2, 0, 0
	v_add_u32_e32 v192, s2, v199
	s_movk_i32 s2, 0x44
	v_lshl_or_b32 v209, v16, 14, v18
	v_mul_lo_u32 v16, v20, s2
	v_exp_f32_e32 v216, v0
	v_exp_f32_e32 v218, v1
	v_exp_f32_e32 v179, v2
	v_exp_f32_e32 v217, v3
	v_exp_f32_e32 v177, v4
	v_exp_f32_e32 v215, v5
	v_exp_f32_e32 v176, v6
	v_exp_f32_e32 v178, v7
	v_exp_f32_e32 v173, v8
	v_exp_f32_e32 v175, v9
	v_exp_f32_e32 v171, v10
	v_exp_f32_e32 v174, v11
	v_exp_f32_e32 v169, v12
	v_exp_f32_e32 v172, v13
	v_exp_f32_e32 v168, v14
	v_exp_f32_e32 v170, v15
	v_add_u32_e32 v0, 0, v19
	s_mov_b32 s2, 0x22000
	v_mov_b32_e32 v182, 0
	v_add3_u32 v190, v0, v16, s2
	v_add_u32_e32 v0, 0, v22
	v_mov_b32_e32 v162, v182
	v_mov_b32_e32 v163, v182
	v_mov_b32_e32 v32, v182
	v_mov_b32_e32 v33, v182
	v_mov_b32_e32 v46, v182
	v_mov_b32_e32 v47, v182
	v_lshl_or_b32 v189, v20, 11, v19
	v_add3_u32 v191, v0, v17, s2
	v_mov_b32_e32 v183, v182
	v_mov_b32_e32 v160, v182
	v_mov_b32_e32 v161, v182
	v_mov_b32_e32 v34, v182
	v_mov_b32_e32 v35, v182
	v_mov_b32_e32 v36, v182
	v_mov_b32_e32 v37, v182
	v_mov_b32_e32 v38, v182
	v_mov_b32_e32 v39, v182
	v_mov_b32_e32 v40, v182
	v_mov_b32_e32 v41, v182
	v_mov_b32_e32 v42, v182
	v_mov_b32_e32 v43, v182
	v_mov_b32_e32 v44, v182
	v_mov_b32_e32 v45, v182
	v_mov_b64_e32 v[62:63], v[46:47]
	v_mov_b64_e32 v[16:17], v[32:33]
	v_mov_b64_e32 v[0:1], v[32:33]
	v_mov_b64_e32 v[166:167], v[162:163]
	s_mov_b32 s36, -1
	s_mul_i32 s59, s33, 6
	s_mov_b32 s64, 2
	s_mov_b64 s[12:13], 0
	s_mov_b32 s62, 0xc3e00000
	v_mov_b32_e32 v211, 0x43e00000
	s_mov_b64 s[28:29], s[16:17]
	s_mov_b64 s[30:31], s[18:19]
	s_mov_b32 s58, 0
	s_mov_b32 s26, 0
	s_mov_b64 s[10:11], 0
	s_mov_b64 s[8:9], 0
	v_mov_b64_e32 v[60:61], v[44:45]
	v_mov_b64_e32 v[58:59], v[42:43]
	v_mov_b64_e32 v[56:57], v[40:41]
	v_mov_b64_e32 v[54:55], v[38:39]
	v_mov_b64_e32 v[52:53], v[36:37]
	v_mov_b64_e32 v[50:51], v[34:35]
	v_mov_b64_e32 v[48:49], v[32:33]
	v_mov_b64_e32 v[18:19], v[34:35]
	v_mov_b64_e32 v[20:21], v[36:37]
	v_mov_b64_e32 v[22:23], v[38:39]
	v_mov_b64_e32 v[24:25], v[40:41]
	v_mov_b64_e32 v[26:27], v[42:43]
	v_mov_b64_e32 v[28:29], v[44:45]
	v_mov_b64_e32 v[30:31], v[46:47]
	v_mov_b64_e32 v[2:3], v[34:35]
	v_mov_b64_e32 v[4:5], v[36:37]
	v_mov_b64_e32 v[6:7], v[38:39]
	v_mov_b64_e32 v[8:9], v[40:41]
	v_mov_b64_e32 v[10:11], v[42:43]
	v_mov_b64_e32 v[12:13], v[44:45]
	v_mov_b64_e32 v[14:15], v[46:47]
	v_mov_b64_e32 v[164:165], v[160:161]
	s_mov_b32 s34, 0
	s_mov_b32 s65, 1
	v_mov_b64_e32 v[184:185], v[182:183]
	v_mov_b32_e32 v81, v80
	v_mov_b32_e32 v82, v80
	v_mov_b32_e32 v83, v80
	v_mov_b32_e32 v84, v80
	v_mov_b32_e32 v85, v80
	v_mov_b32_e32 v86, v80
	v_mov_b32_e32 v87, v80
	v_mov_b32_e32 v88, v80
	v_mov_b32_e32 v89, v80
	v_mov_b32_e32 v90, v80
	v_mov_b32_e32 v91, v80
	v_mov_b32_e32 v92, v80
	v_mov_b32_e32 v93, v80
	v_mov_b32_e32 v94, v80
	v_mov_b32_e32 v95, v80
	v_mov_b32_e32 v255, 0x3f600000
	s_mov_b32 s93, 0x3b000000
	v_mbcnt_lo_u32_b32 v253, -1, 0
	v_mbcnt_hi_u32_b32 v253, -1, v253
	v_lshrrev_b32_e32 v253, 5, v253
	v_mul_u32_u24_e32 v253, 0x700, v253
	v_add_u32_e32 v253, v253, v192

; DI void finishSM(f32x16& p0, f32x16& p1, float alpha, float& l_reg, bf16x8& pa0, bf16x8& pa1, bf16x8& pa2, bf16x8& pa3) {
; #pragma unroll
;     for (int r = 0; r < 16; ++r) p1[r] = __builtin_amdgcn_exp2f(p1[r]);
;     float ps = 0;
; #pragma unroll
;     for (int r = 0; r < 16; ++r) ps += p0[r];
; #pragma unroll
;     for (int r = 0; r < 16; ++r) ps += p1[r];
;     { auto rr = __builtin_amdgcn_permlane32_swap(__float_as_uint(ps), __float_as_uint(ps), false, false); ps = __uint_as_float(rr[0]) + __uint_as_float(rr[1]); }
;     l_reg = l_reg * alpha + ps;
;     ...
;     AT_PK4(p0, 0, pa0); AT_PK4(p0, 8, pa1); AT_PK4(p1, 0, pa2); AT_PK4(p1, 8, pa3);
;     ...
; }
; DI void qkt(f32x16& p0, f32x16& p1, const char* Ks, const bf16x8* qr, const f32x16& negm, int r32, int hi) {
; #pragma unroll
;     for (int d0 = 0; d0 < 4; ++d0) { const int cb = (d0 * 16 + hi * 8) * 2;
;         const bf16x8 b0 = *reinterpret_cast<const bf16x8*>(Ks + AT_KSWZ(r32, cb));
;         const bf16x8 b1 = *reinterpret_cast<const bf16x8*>(Ks + AT_KSWZ(32 + r32, cb));
;         p0 = __builtin_amdgcn_mfma_f32_32x32x16_bf16(b0, qr[d0], d0 == 0 ? negm : p0, 0, 0, 0);
;         p1 = __builtin_amdgcn_mfma_f32_32x32x16_bf16(b1, qr[d0], d0 == 0 ? negm : p1, 0, 0, 0); }
.LBB4_702:
	s_lshl_b32 s26, s66, 13
	s_add_i32 s26, s26, 0
	v_add_u32_e32 v72, s26, v205
	v_add_u32_e32 v112, s26, v206
	v_add_u32_e32 v180, s26, v207
	s_waitcnt lgkmcnt(1)
	v_mfma_f32_32x32x16_bf16 v[128:143], v[64:67], v[156:159], v[80:95]
	ds_read_b128 v[64:67], v72 offset:49152
	ds_read_b128 v[72:75], v72 offset:53248
	ds_read_b128 v[76:79], v112 offset:49152
	ds_read_b128 v[220:223], v112 offset:53248
	v_exp_f32_e32 v186, v97
	v_exp_f32_e32 v213, v98
	v_exp_f32_e32 v214, v99
	v_exp_f32_e32 v219, v100
	v_exp_f32_e32 v228, v101
	s_waitcnt lgkmcnt(4)
	v_mfma_f32_32x32x16_bf16 v[112:127], v[68:71], v[156:159], v[80:95]
	ds_read_b128 v[68:71], v180 offset:49152
	ds_read_b128 v[224:227], v180 offset:53248
	v_exp_f32_e32 v180, v96
	v_cvt_pk_bf16_f32 v96, v216, v218
	v_cvt_pk_bf16_f32 v97, v179, v217
	v_cvt_pk_bf16_f32 v98, v177, v215
	v_cvt_pk_bf16_f32 v99, v176, v178
	s_waitcnt lgkmcnt(4)
	v_mfma_f32_32x32x16_bf16 v[112:127], v[72:75], v[152:155], v[112:127]
	v_add_f32_e32 v75, 0, v216
	v_add_f32_e32 v75, v218, v75
	v_add_f32_e32 v75, v179, v75
	v_add_f32_e32 v75, v217, v75
	v_add_f32_e32 v75, v177, v75
	v_add_f32_e32 v75, v215, v75
	v_add_f32_e32 v75, v176, v75
	v_mfma_f32_32x32x16_bf16 v[128:143], v[64:67], v[152:155], v[128:143]
	v_add_f32_e32 v75, v178, v75
	v_add_f32_e32 v75, v173, v75
	v_add_f32_e32 v75, v175, v75
	v_add_f32_e32 v75, v171, v75
	v_add_f32_e32 v75, v174, v75
	v_add_f32_e32 v75, v169, v75
	v_add_f32_e32 v75, v172, v75
	s_waitcnt lgkmcnt(3)
	v_mfma_f32_32x32x16_bf16 v[128:143], v[76:79], v[148:151], v[128:143]
	v_add_f32_e32 v75, v168, v75
	v_add_f32_e32 v75, v170, v75
	v_add_f32_e32 v75, v180, v75
	v_add_f32_e32 v75, v186, v75
	v_exp_f32_e32 v64, v102
	v_exp_f32_e32 v65, v103
	v_exp_f32_e32 v66, v104
	s_waitcnt lgkmcnt(2)
	v_mfma_f32_32x32x16_bf16 v[112:127], v[220:223], v[148:151], v[112:127]
	v_exp_f32_e32 v67, v105
	v_exp_f32_e32 v105, v106
	v_exp_f32_e32 v106, v107
	v_exp_f32_e32 v107, v108
	v_exp_f32_e32 v72, v109
	v_exp_f32_e32 v73, v110
	v_exp_f32_e32 v74, v111
	s_waitcnt lgkmcnt(1)
	v_mfma_f32_32x32x16_bf16 v[128:143], v[68:71], v[144:147], v[128:143]
	v_add_f32_e32 v68, v213, v75
	v_add_f32_e32 v68, v214, v68
	v_add_f32_e32 v68, v219, v68
	v_add_f32_e32 v68, v228, v68
	v_add_f32_e32 v68, v64, v68
	v_add_f32_e32 v68, v65, v68
	v_add_f32_e32 v68, v66, v68
	v_add_f32_e32 v68, v67, v68
	s_waitcnt lgkmcnt(0)
	v_mfma_f32_32x32x16_bf16 v[112:127], v[224:227], v[144:147], v[112:127]
	v_add_f32_e32 v68, v105, v68
	v_add_f32_e32 v68, v106, v68
	v_add_f32_e32 v68, v107, v68
	v_add_f32_e32 v68, v72, v68
	v_add_f32_e32 v68, v73, v68
	v_add_f32_e32 v183, v74, v68
	v_mov_b32_e32 v212, v183
	v_cvt_pk_bf16_f32 v108, v173, v175
	v_cvt_pk_bf16_f32 v109, v171, v174
	v_cvt_pk_bf16_f32 v110, v169, v172
	v_cvt_pk_bf16_f32 v111, v168, v170
	v_cvt_pk_bf16_f32 v100, v180, v186
	v_cvt_pk_bf16_f32 v101, v213, v214
	v_cvt_pk_bf16_f32 v102, v219, v228
	v_cvt_pk_bf16_f32 v103, v64, v65
	v_cvt_pk_bf16_f32 v104, v66, v67
	v_cvt_pk_bf16_f32 v105, v105, v106
	v_cvt_pk_bf16_f32 v106, v107, v72
	v_cvt_pk_bf16_f32 v107, v73, v74
	s_nop 1
	v_permlane32_swap_b32_e32 v183, v212
	s_add_u32 s74, s46, s28
	s_addc_u32 s75, s47, s29
	s_add_u32 s78, s74, 0x23808000
	s_addc_u32 s79, s75, 0
	s_add_u32 s80, s74, 0x2380a000
	s_addc_u32 s81, s75, 0
	s_add_u32 s76, s46, s30
	s_addc_u32 s77, s47, s31
	s_add_u32 s82, s76, 0x21804000
	s_addc_u32 s83, s77, 0
	global_load_dwordx4 v[176:179], v197, s[78:79]
	global_load_dwordx4 v[172:175], v197, s[80:81]
	global_load_dwordx4 v[168:171], v198, s[82:83]
	s_andn2_b64 vcc, exec, s[2:3]
	s_cbranch_vccnz .LBB4_704
	s_mov_b64 s[2:3], s[8:9]
	global_store_dwordx2 v189, v[184:185], s[2:3] nt
; #define AT_SBAR() __builtin_amdgcn_sched_barrier(0)
; template <int OFF> DI s16x4 tr_read(int vb) { s16x4 r; asm volatile("ds_read_b64_tr_b16 %0, %1 offset:%2" : "=&v"(r) : "v"(vb), "i"(OFF) : "memory"); return r; }
; template <int D0> DI void pv_one(f32x16& od, int vb, bf16x8 pa0, bf16x8 pa1, bf16x8 pa2, bf16x8 pa3) {
;     const s16x4 l0 = tr_read<v_rd_off(D0, 0, 0)>(vb), h0 = tr_read<v_rd_off(D0, 0, 1)>(vb), l1 = tr_read<v_rd_off(D0, 1, 0)>(vb), h1 = tr_read<v_rd_off(D0, 1, 1)>(vb);
;     const s16x4 l2 = tr_read<v_rd_off(D0, 2, 0)>(vb), h2 = tr_read<v_rd_off(D0, 2, 1)>(vb), l3 = tr_read<v_rd_off(D0, 3, 0)>(vb), h3 = tr_read<v_rd_off(D0, 3, 1)>(vb);
;     asm volatile("s_waitcnt lgkmcnt(0)" ::: "memory"); AT_SBAR();
;     ...
;     od = __builtin_amdgcn_mfma_f32_32x32x16_bf16(AT_PK(l0, h0), pa0, od, 0, 0, 0);
;     od = __builtin_amdgcn_mfma_f32_32x32x16_bf16(AT_PK(l1, h1), pa1, od, 0, 0, 0);
;     od = __builtin_amdgcn_mfma_f32_32x32x16_bf16(AT_PK(l2, h2), pa2, od, 0, 0, 0);
;     od = __builtin_amdgcn_mfma_f32_32x32x16_bf16(AT_PK(l3, h3), pa3, od, 0, 0, 0);
;     ...
; }
; DI void pv_all_sm(f32x16* o, int vb, bf16x8 pa0, bf16x8 pa1, bf16x8 pa2, bf16x8 pa3, f32x16& p0, f32x16& p1, float& m_ref, f32x16& negm, float& alpha) {
;     pv_one<0>(o[0], vb, pa0, pa1, pa2, pa3);
;     float pmax = p0[0];
; #pragma unroll
;     for (int r = 1; r < 16; ++r) pmax = fmaxf(pmax, p0[r]);
;     pv_one<1>(o[1], vb, pa0, pa1, pa2, pa3);
; #pragma unroll
;     for (int r = 0; r < 16; ++r) pmax = fmaxf(pmax, p1[r]);
;     { auto rr = __builtin_amdgcn_permlane32_swap(__float_as_uint(pmax), __float_as_uint(pmax), false, false); pmax = fmaxf(__uint_as_float(rr[0]), __uint_as_float(rr[1])); }
;     pv_one<2>(o[2], vb, pa0, pa1, pa2, pa3);
;     alpha = 1.f;
;     if (__builtin_expect(!__all(pmax <= THRL), 0)) {
;         const float dl = fmaxf(pmax, 0.f); m_ref += dl; alpha = __builtin_amdgcn_exp2f(-dl);
; #pragma unroll
;         for (int r = 0; r < 16; ++r) { p0[r] -= dl; p1[r] -= dl; }
; #pragma unroll
;         for (int r = 0; r < 16; ++r) negm[r] = -m_ref;
;     }
;     pv_one<3>(o[3], vb, pa0, pa1, pa2, pa3);
; #pragma unroll
;     for (int r = 0; r < 16; ++r) p0[r] = __builtin_amdgcn_exp2f(p0[r]);
; }
.LBB4_704:
	s_lshl_b32 s67, s65, 14
	v_add_u32_e32 v186, s67, v253
	ds_read_b64_tr_b16 v[64:65], v186 offset:0
	ds_read_b64_tr_b16 v[66:67], v186 offset:0x100
	ds_read_b64_tr_b16 v[68:69], v186 offset:0x1000
	ds_read_b64_tr_b16 v[70:71], v186 offset:0x1100
	ds_read_b64_tr_b16 v[72:73], v186 offset:0x2000
	ds_read_b64_tr_b16 v[74:75], v186 offset:0x2100
	ds_read_b64_tr_b16 v[76:77], v186 offset:0x3000
	ds_read_b64_tr_b16 v[78:79], v186 offset:0x3100
	s_waitcnt lgkmcnt(0)
	s_nop 0
	v_mfma_f32_32x32x16_bf16 v[32:47], v[64:67], v[96:99], v[32:47]
	v_max_f32_e32 v64, v128, v129
	v_max3_f32 v64, v64, v130, v131
	v_max3_f32 v64, v64, v132, v133
	v_max3_f32 v64, v64, v134, v135
	v_max3_f32 v64, v64, v136, v137
	v_mfma_f32_32x32x16_bf16 v[32:47], v[68:71], v[108:111], v[32:47]
	v_max3_f32 v64, v64, v138, v139
	v_max3_f32 v66, v64, v140, v141
	ds_read_b64_tr_b16 v[64:65], v186 offset:0x200
	v_max3_f32 v180, v66, v142, v143
	ds_read_b64_tr_b16 v[66:67], v186 offset:0x300
	ds_read_b64_tr_b16 v[68:69], v186 offset:0x1200
	ds_read_b64_tr_b16 v[70:71], v186 offset:0x1300
	v_mfma_f32_32x32x16_bf16 v[32:47], v[72:75], v[100:103], v[32:47]
	ds_read_b64_tr_b16 v[72:73], v186 offset:0x2200
	ds_read_b64_tr_b16 v[74:75], v186 offset:0x2300
	ds_read_b64_tr_b16 v[214:215], v186 offset:0x3200
	ds_read_b64_tr_b16 v[216:217], v186 offset:0x3300
	s_waitcnt lgkmcnt(0)
	v_mfma_f32_32x32x16_bf16 v[32:47], v[76:79], v[104:107], v[32:47]
	v_mfma_f32_32x32x16_bf16 v[48:63], v[64:67], v[96:99], v[48:63]
	v_max3_f32 v76, v180, v112, v113
	v_max3_f32 v64, v76, v114, v115
	ds_read_b64_tr_b16 v[66:67], v186 offset:0x400
	v_max3_f32 v64, v64, v116, v117
	v_max3_f32 v64, v64, v118, v119
	v_max3_f32 v64, v64, v120, v121
	v_max3_f32 v64, v64, v122, v123
	v_mfma_f32_32x32x16_bf16 v[48:63], v[68:71], v[108:111], v[48:63]
	ds_read_b64_tr_b16 v[68:69], v186 offset:0x500
	ds_read_b64_tr_b16 v[70:71], v186 offset:0x1400
	v_max3_f32 v64, v64, v124, v125
	v_max3_f32 v64, v64, v126, v127
	v_mov_b32_e32 v65, v64
	s_nop 1
	v_permlane32_swap_b32_e32 v64, v65
	v_mfma_f32_32x32x16_bf16 v[48:63], v[72:75], v[100:103], v[48:63]
	ds_read_b64_tr_b16 v[72:73], v186 offset:0x1500
	ds_read_b64_tr_b16 v[74:75], v186 offset:0x2400
	ds_read_b64_tr_b16 v[76:77], v186 offset:0x2500
	ds_read_b64_tr_b16 v[218:219], v186 offset:0x3400
	ds_read_b64_tr_b16 v[220:221], v186 offset:0x3500
	s_waitcnt lgkmcnt(0)
	v_mfma_f32_32x32x16_bf16 v[48:63], v[214:217], v[104:107], v[48:63]
	v_max_f32_e32 v64, v64, v65
	v_mfma_f32_32x32x16_bf16 v[16:31], v[66:69], v[96:99], v[16:31]
	v_cmp_ge_f32_e32 vcc, s25, v64
	s_cmp_eq_u64 vcc, exec
	v_mfma_f32_32x32x16_bf16 v[16:31], v[70:73], v[108:111], v[16:31]
	v_mfma_f32_32x32x16_bf16 v[16:31], v[74:77], v[100:103], v[16:31]
	v_mfma_f32_32x32x16_bf16 v[16:31], v[218:221], v[104:107], v[16:31]
	s_cbranch_scc0 .LBB4_737
	v_mov_b32_e32 v180, 1.0
.LBB4_706:
	ds_read_b64_tr_b16 v[214:215], v186 offset:0x600
	ds_read_b64_tr_b16 v[216:217], v186 offset:0x700
	ds_read_b64_tr_b16 v[218:219], v186 offset:0x1600
	ds_read_b64_tr_b16 v[220:221], v186 offset:0x1700
	ds_read_b64_tr_b16 v[222:223], v186 offset:0x2600
	ds_read_b64_tr_b16 v[224:225], v186 offset:0x2700
	ds_read_b64_tr_b16 v[226:227], v186 offset:0x3600
	ds_read_b64_tr_b16 v[228:229], v186 offset:0x3700
	s_waitcnt lgkmcnt(0)
	s_nop 0
	v_mfma_f32_32x32x16_bf16 v[0:15], v[214:217], v[96:99], v[0:15]
	s_lshl_b32 s2, s64, 14
	s_add_i32 s2, s2, 0
	s_lshl_b32 s3, s64, 13
	v_add_u32_e32 v96, s2, v200
	s_sub_i32 s78, s2, s3
	s_waitcnt vmcnt(0)
	v_add_u32_e32 v97, s2, v201
	v_mfma_f32_32x32x16_bf16 v[0:15], v[218:221], v[108:111], v[0:15]
	ds_write_b128 v96, v[176:179]
	v_add_u32_e32 v96, s78, v202
	ds_write_b128 v97, v[172:175]
	ds_write_b128 v96, v[168:171] offset:49152
	s_andn2_b64 s[2:3], exec, s[34:35]
	s_andn2_b64 vcc, exec, s[34:35]
	v_mfma_f32_32x32x16_bf16 v[0:15], v[222:225], v[100:103], v[0:15]
	v_mfma_f32_32x32x16_bf16 v[0:15], v[226:229], v[104:107], v[0:15]
	s_cbranch_vccnz .LBB4_711
	v_med3_f32 v97, v160, -v255, v255
	v_med3_f32 v98, v164, -v255, v255
	v_cvt_scalef32_pk_fp8_f32 v99, v97, v98, s93
	v_med3_f32 v97, v161, -v255, v255
	v_med3_f32 v98, v165, -v255, v255
	v_cvt_scalef32_pk_fp8_f32 v100, v97, v98, s93
	v_med3_f32 v97, v162, -v255, v255
	v_med3_f32 v98, v166, -v255, v255
	s_bitcmp1_b32 s58, 0
	v_cvt_scalef32_pk_fp8_f32 v101, v97, v98, s93
	s_cselect_b32 s8, 0x1100, 0
	v_med3_f32 v97, v163, -v255, v255
	v_med3_f32 v98, v167, -v255, v255
	v_cmp_eq_u32_e32 vcc, 0, v181
	v_add_u32_e32 v96, s8, v191
	v_cvt_scalef32_pk_fp8_f32 v102, v97, v98, s93
	s_and_b64 vcc, exec, vcc
	s_and_b32 s34, s58, 31
	ds_write_b16 v96, v99
	ds_write_b16 v96, v100 offset:68
	ds_write_b16 v96, v101 offset:136
	ds_write_b16 v96, v102 offset:204
	s_cbranch_vccnz .LBB4_735
	s_lshl_b32 s8, s34, 7
	s_lshl_b32 s9, s58, 6
	s_and_b32 s8, s8, 0xf00
	s_and_b32 s9, s9, 64
	s_or_b32 s26, s8, s9
	s_cbranch_execnz .LBB4_710

; DI void finishSM(f32x16& p0, f32x16& p1, float alpha, float& l_reg, bf16x8& pa0, bf16x8& pa1, bf16x8& pa2, bf16x8& pa3) {
; #pragma unroll
;     for (int r = 0; r < 16; ++r) p1[r] = __builtin_amdgcn_exp2f(p1[r]);
;     float ps = 0;
; #pragma unroll
;     for (int r = 0; r < 16; ++r) ps += p0[r];
; #pragma unroll
;     for (int r = 0; r < 16; ++r) ps += p1[r];
;     { auto rr = __builtin_amdgcn_permlane32_swap(__float_as_uint(ps), __float_as_uint(ps), false, false); ps = __uint_as_float(rr[0]) + __uint_as_float(rr[1]); }
;     l_reg = l_reg * alpha + ps;
;     ...
;     AT_PK4(p0, 0, pa0); AT_PK4(p0, 8, pa1); AT_PK4(p1, 0, pa2); AT_PK4(p1, 8, pa3);
;     ...
; }
; DI void qkt(f32x16& p0, f32x16& p1, const char* Ks, const bf16x8* qr, const f32x16& negm, int r32, int hi) {
; #pragma unroll
;     for (int d0 = 0; d0 < 4; ++d0) { const int cb = (d0 * 16 + hi * 8) * 2;
;         const bf16x8 b0 = *reinterpret_cast<const bf16x8*>(Ks + AT_KSWZ(r32, cb));
;         const bf16x8 b1 = *reinterpret_cast<const bf16x8*>(Ks + AT_KSWZ(32 + r32, cb));
;         p0 = __builtin_amdgcn_mfma_f32_32x32x16_bf16(b0, qr[d0], d0 == 0 ? negm : p0, 0, 0, 0);
;         p1 = __builtin_amdgcn_mfma_f32_32x32x16_bf16(b1, qr[d0], d0 == 0 ? negm : p1, 0, 0, 0); }
.LBB4_723:
	v_exp_f32_e32 v186, v128
	v_exp_f32_e32 v230, v129
	v_exp_f32_e32 v231, v130
	v_exp_f32_e32 v232, v131
	v_exp_f32_e32 v233, v132
	v_exp_f32_e32 v234, v133
	v_exp_f32_e32 v235, v134
	v_exp_f32_e32 v236, v135
	v_exp_f32_e32 v237, v136
	v_exp_f32_e32 v238, v137
	v_exp_f32_e32 v239, v138
	v_exp_f32_e32 v240, v139
	v_exp_f32_e32 v241, v140
	v_exp_f32_e32 v242, v141
	v_exp_f32_e32 v243, v142
	v_exp_f32_e32 v244, v143
	v_add_u32_e32 v101, s78, v205
	v_add_u32_e32 v102, s78, v206
	v_add_u32_e32 v103, s78, v207
	ds_read_b128 v[172:175], v101 offset:49152
	ds_read_b128 v[176:179], v101 offset:53248
	ds_read_b128 v[214:217], v102 offset:49152
	ds_read_b128 v[218:221], v102 offset:53248
	ds_read_b128 v[222:225], v103 offset:49152
	ds_read_b128 v[226:229], v103 offset:53248
	v_exp_f32_e32 v112, v112
	v_exp_f32_e32 v113, v113
	v_exp_f32_e32 v114, v114
	s_waitcnt lgkmcnt(7)
	v_mfma_f32_32x32x16_bf16 v[128:143], v[96:99], v[156:159], v[80:95]
	v_exp_f32_e32 v115, v115
	v_exp_f32_e32 v116, v116
	v_exp_f32_e32 v117, v117
	v_exp_f32_e32 v118, v118
	v_exp_f32_e32 v119, v119
	s_waitcnt lgkmcnt(6)
	v_mfma_f32_32x32x16_bf16 v[96:111], v[168:171], v[156:159], v[80:95]
	v_exp_f32_e32 v168, v120
	v_add_f32_e32 v120, 0, v186
	v_add_f32_e32 v120, v230, v120
	v_add_f32_e32 v120, v231, v120
	v_add_f32_e32 v120, v232, v120
	v_add_f32_e32 v120, v233, v120
	v_add_f32_e32 v120, v234, v120
	v_add_f32_e32 v120, v235, v120
	v_add_f32_e32 v120, v236, v120
	v_add_f32_e32 v120, v237, v120
	v_add_f32_e32 v120, v238, v120
	s_waitcnt lgkmcnt(5)
	v_mfma_f32_32x32x16_bf16 v[128:143], v[172:175], v[152:155], v[128:143]
	v_add_f32_e32 v120, v239, v120
	v_add_f32_e32 v120, v240, v120
	v_add_f32_e32 v120, v241, v120
	v_add_f32_e32 v120, v242, v120
	v_add_f32_e32 v120, v243, v120
	v_add_f32_e32 v120, v244, v120
	v_add_f32_e32 v120, v112, v120
	s_waitcnt lgkmcnt(4)
	v_mfma_f32_32x32x16_bf16 v[96:111], v[176:179], v[152:155], v[96:111]
	v_add_f32_e32 v120, v113, v120
	v_add_f32_e32 v120, v114, v120
	v_add_f32_e32 v120, v115, v120
	v_add_f32_e32 v120, v116, v120
	v_exp_f32_e32 v169, v121
	v_add_f32_e32 v120, v117, v120
	v_exp_f32_e32 v170, v122
	s_waitcnt lgkmcnt(3)
	v_mfma_f32_32x32x16_bf16 v[128:143], v[214:217], v[148:151], v[128:143]
	v_add_f32_e32 v120, v118, v120
	v_exp_f32_e32 v171, v123
	v_add_f32_e32 v120, v119, v120
	v_exp_f32_e32 v172, v124
	v_add_f32_e32 v120, v168, v120
	v_exp_f32_e32 v173, v125
	v_add_f32_e32 v120, v169, v120
	s_waitcnt lgkmcnt(2)
	v_mfma_f32_32x32x16_bf16 v[96:111], v[218:221], v[148:151], v[96:111]
	v_exp_f32_e32 v174, v126
	v_add_f32_e32 v120, v170, v120
	v_exp_f32_e32 v175, v127
	v_add_f32_e32 v120, v171, v120
	v_add_f32_e32 v120, v172, v120
	v_add_f32_e32 v120, v173, v120
	v_add_f32_e32 v120, v174, v120
	s_waitcnt lgkmcnt(1)
	v_mfma_f32_32x32x16_bf16 v[128:143], v[222:225], v[144:147], v[128:143]
	v_add_f32_e32 v213, v175, v120
	v_mov_b32_e32 v214, v213
	v_cvt_pk_bf16_f32 v120, v186, v230
	v_cvt_pk_bf16_f32 v121, v231, v232
	v_cvt_pk_bf16_f32 v122, v233, v234
	v_cvt_pk_bf16_f32 v123, v235, v236
	v_cvt_pk_bf16_f32 v124, v237, v238
	s_waitcnt lgkmcnt(0)
	v_mfma_f32_32x32x16_bf16 v[96:111], v[226:229], v[144:147], v[96:111]
	v_cvt_pk_bf16_f32 v125, v239, v240
	v_cvt_pk_bf16_f32 v126, v241, v242
	v_cvt_pk_bf16_f32 v127, v243, v244
	v_cvt_pk_bf16_f32 v112, v112, v113
	v_cvt_pk_bf16_f32 v113, v114, v115
	v_cvt_pk_bf16_f32 v114, v116, v117
	v_cvt_pk_bf16_f32 v115, v118, v119
	v_cvt_pk_bf16_f32 v116, v168, v169
	v_cvt_pk_bf16_f32 v117, v170, v171
	v_cvt_pk_bf16_f32 v118, v172, v173
	v_cvt_pk_bf16_f32 v119, v174, v175
	v_permlane32_swap_b32_e32 v213, v214
	s_add_u32 s78, s74, 0x2380c000
	s_addc_u32 s79, s75, 0
	s_add_u32 s74, s74, 0x2380e000
	s_addc_u32 s75, s75, 0
	s_add_u32 s76, s76, 0x21806000
	s_addc_u32 s77, s77, 0
	global_load_dwordx4 v[176:179], v197, s[78:79]
	global_load_dwordx4 v[172:175], v197, s[74:75]
	s_nop 0
	global_load_dwordx4 v[168:171], v198, s[76:77]
	s_and_b64 vcc, exec, s[2:3]
	s_cbranch_vccnz .LBB4_725
	s_mov_b64 s[2:3], s[8:9]
	global_store_dwordx2 v189, v[184:185], s[2:3] nt
; #define AT_SBAR() __builtin_amdgcn_sched_barrier(0)
; template <int OFF> DI s16x4 tr_read(int vb) { s16x4 r; asm volatile("ds_read_b64_tr_b16 %0, %1 offset:%2" : "=&v"(r) : "v"(vb), "i"(OFF) : "memory"); return r; }
; template <int D0> DI void pv_one(f32x16& od, int vb, bf16x8 pa0, bf16x8 pa1, bf16x8 pa2, bf16x8 pa3) {
;     const s16x4 l0 = tr_read<v_rd_off(D0, 0, 0)>(vb), h0 = tr_read<v_rd_off(D0, 0, 1)>(vb), l1 = tr_read<v_rd_off(D0, 1, 0)>(vb), h1 = tr_read<v_rd_off(D0, 1, 1)>(vb);
;     const s16x4 l2 = tr_read<v_rd_off(D0, 2, 0)>(vb), h2 = tr_read<v_rd_off(D0, 2, 1)>(vb), l3 = tr_read<v_rd_off(D0, 3, 0)>(vb), h3 = tr_read<v_rd_off(D0, 3, 1)>(vb);
;     asm volatile("s_waitcnt lgkmcnt(0)" ::: "memory"); AT_SBAR();
;     ...
;     od = __builtin_amdgcn_mfma_f32_32x32x16_bf16(AT_PK(l0, h0), pa0, od, 0, 0, 0);
;     od = __builtin_amdgcn_mfma_f32_32x32x16_bf16(AT_PK(l1, h1), pa1, od, 0, 0, 0);
;     od = __builtin_amdgcn_mfma_f32_32x32x16_bf16(AT_PK(l2, h2), pa2, od, 0, 0, 0);
;     od = __builtin_amdgcn_mfma_f32_32x32x16_bf16(AT_PK(l3, h3), pa3, od, 0, 0, 0);
;     ...
; }
; DI void pv_all_sm(f32x16* o, int vb, bf16x8 pa0, bf16x8 pa1, bf16x8 pa2, bf16x8 pa3, f32x16& p0, f32x16& p1, float& m_ref, f32x16& negm, float& alpha) {
;     pv_one<0>(o[0], vb, pa0, pa1, pa2, pa3);
;     float pmax = p0[0];
; #pragma unroll
;     for (int r = 1; r < 16; ++r) pmax = fmaxf(pmax, p0[r]);
;     pv_one<1>(o[1], vb, pa0, pa1, pa2, pa3);
; #pragma unroll
;     for (int r = 0; r < 16; ++r) pmax = fmaxf(pmax, p1[r]);
;     { auto rr = __builtin_amdgcn_permlane32_swap(__float_as_uint(pmax), __float_as_uint(pmax), false, false); pmax = fmaxf(__uint_as_float(rr[0]), __uint_as_float(rr[1])); }
;     pv_one<2>(o[2], vb, pa0, pa1, pa2, pa3);
;     alpha = 1.f;
;     if (__builtin_expect(!__all(pmax <= THRL), 0)) {
;         const float dl = fmaxf(pmax, 0.f); m_ref += dl; alpha = __builtin_amdgcn_exp2f(-dl);
; #pragma unroll
;         for (int r = 0; r < 16; ++r) { p0[r] -= dl; p1[r] -= dl; }
; #pragma unroll
;         for (int r = 0; r < 16; ++r) negm[r] = -m_ref;
;     }
;     pv_one<3>(o[3], vb, pa0, pa1, pa2, pa3);
; #pragma unroll
;     for (int r = 0; r < 16; ++r) p0[r] = __builtin_amdgcn_exp2f(p0[r]);
; }
.LBB4_725:
	v_lshl_add_u32 v215, s66, 14, v253
	ds_read_b64_tr_b16 v[216:217], v215 offset:0
	ds_read_b64_tr_b16 v[218:219], v215 offset:0x100
	ds_read_b64_tr_b16 v[220:221], v215 offset:0x1000
	ds_read_b64_tr_b16 v[222:223], v215 offset:0x1100
	ds_read_b64_tr_b16 v[224:225], v215 offset:0x2000
	ds_read_b64_tr_b16 v[226:227], v215 offset:0x2100
	ds_read_b64_tr_b16 v[228:229], v215 offset:0x3000
	ds_read_b64_tr_b16 v[230:231], v215 offset:0x3100
	s_waitcnt lgkmcnt(0)
	s_nop 0
	v_mfma_f32_32x32x16_bf16 v[32:47], v[216:219], v[120:123], v[32:47]
	v_max_f32_e32 v186, v128, v129
	ds_read_b64_tr_b16 v[216:217], v215 offset:0x200
	ds_read_b64_tr_b16 v[218:219], v215 offset:0x300
	v_max3_f32 v186, v186, v130, v131
	v_max3_f32 v186, v186, v132, v133
	v_mfma_f32_32x32x16_bf16 v[32:47], v[220:223], v[124:127], v[32:47]
	ds_read_b64_tr_b16 v[220:221], v215 offset:0x1200
	ds_read_b64_tr_b16 v[222:223], v215 offset:0x1300
	v_max3_f32 v186, v186, v134, v135
	v_max3_f32 v186, v186, v136, v137
	v_max3_f32 v186, v186, v138, v139
	v_max3_f32 v186, v186, v140, v141
	v_max3_f32 v186, v186, v142, v143
	v_mfma_f32_32x32x16_bf16 v[32:47], v[224:227], v[112:115], v[32:47]
	ds_read_b64_tr_b16 v[224:225], v215 offset:0x2200
	ds_read_b64_tr_b16 v[226:227], v215 offset:0x2300
	ds_read_b64_tr_b16 v[232:233], v215 offset:0x3200
	ds_read_b64_tr_b16 v[234:235], v215 offset:0x3300
	s_waitcnt lgkmcnt(0)
	v_mfma_f32_32x32x16_bf16 v[32:47], v[228:231], v[116:119], v[32:47]
	v_mfma_f32_32x32x16_bf16 v[48:63], v[216:219], v[120:123], v[48:63]
	v_max3_f32 v186, v186, v96, v97
	v_max3_f32 v186, v186, v98, v99
	ds_read_b64_tr_b16 v[218:219], v215 offset:0x400
	v_max3_f32 v186, v186, v100, v101
	v_max3_f32 v186, v186, v102, v103
	v_max3_f32 v186, v186, v104, v105
	v_max3_f32 v186, v186, v106, v107
	v_mfma_f32_32x32x16_bf16 v[48:63], v[220:223], v[124:127], v[48:63]
	ds_read_b64_tr_b16 v[220:221], v215 offset:0x500
	ds_read_b64_tr_b16 v[222:223], v215 offset:0x1400
	v_max3_f32 v186, v186, v108, v109
	v_max3_f32 v186, v186, v110, v111
	v_mov_b32_e32 v216, v186
	s_nop 1
	v_permlane32_swap_b32_e32 v186, v216
	v_mfma_f32_32x32x16_bf16 v[48:63], v[224:227], v[112:115], v[48:63]
	ds_read_b64_tr_b16 v[224:225], v215 offset:0x1500
	ds_read_b64_tr_b16 v[226:227], v215 offset:0x2400
	ds_read_b64_tr_b16 v[228:229], v215 offset:0x2500
	ds_read_b64_tr_b16 v[236:237], v215 offset:0x3400
	ds_read_b64_tr_b16 v[238:239], v215 offset:0x3500
	s_waitcnt lgkmcnt(0)
	v_mfma_f32_32x32x16_bf16 v[48:63], v[232:235], v[116:119], v[48:63]
	v_max_f32_e32 v216, v186, v216
	v_mfma_f32_32x32x16_bf16 v[16:31], v[218:221], v[120:123], v[16:31]
	v_cmp_ge_f32_e32 vcc, s25, v216
	s_cmp_eq_u64 vcc, exec
	v_mov_b32_e32 v186, 1.0
	v_mfma_f32_32x32x16_bf16 v[16:31], v[222:225], v[124:127], v[16:31]
	v_mfma_f32_32x32x16_bf16 v[16:31], v[226:229], v[112:115], v[16:31]
	v_mfma_f32_32x32x16_bf16 v[16:31], v[236:239], v[116:119], v[16:31]
	s_cbranch_scc0 .LBB4_738
.LBB4_726:
	ds_read_b64_tr_b16 v[216:217], v215 offset:0x600
	ds_read_b64_tr_b16 v[218:219], v215 offset:0x700
	ds_read_b64_tr_b16 v[220:221], v215 offset:0x1600
	ds_read_b64_tr_b16 v[222:223], v215 offset:0x1700
	ds_read_b64_tr_b16 v[224:225], v215 offset:0x2600
	ds_read_b64_tr_b16 v[226:227], v215 offset:0x2700
	ds_read_b64_tr_b16 v[228:229], v215 offset:0x3600
	ds_read_b64_tr_b16 v[230:231], v215 offset:0x3700
	s_waitcnt lgkmcnt(0)
	s_nop 0
	v_mfma_f32_32x32x16_bf16 v[0:15], v[216:219], v[120:123], v[0:15]
	s_add_i32 s2, s67, 0
	v_add_u32_e32 v120, s2, v200
	s_waitcnt vmcnt(0)
	ds_write_b128 v120, v[176:179]
	s_mov_b32 s26, 0
	s_andn2_b64 vcc, exec, s[34:35]
	v_mfma_f32_32x32x16_bf16 v[0:15], v[220:223], v[124:127], v[0:15]
	v_mfma_f32_32x32x16_bf16 v[0:15], v[224:227], v[112:115], v[0:15]
	v_add_u32_e32 v112, s2, v201
	ds_write_b128 v112, v[172:175]
	v_lshl_add_u32 v112, s65, 13, v203
	ds_write_b128 v112, v[168:171] offset:49152
	s_andn2_b64 s[2:3], exec, s[34:35]
	v_mfma_f32_32x32x16_bf16 v[0:15], v[228:231], v[116:119], v[0:15]
	s_cbranch_vccnz .LBB4_731
	v_med3_f32 v113, v160, -v255, v255
	v_med3_f32 v114, v164, -v255, v255
	v_cvt_scalef32_pk_fp8_f32 v115, v113, v114, s93
	v_med3_f32 v113, v161, -v255, v255
	v_med3_f32 v114, v165, -v255, v255
	v_cvt_scalef32_pk_fp8_f32 v116, v113, v114, s93
	v_med3_f32 v113, v162, -v255, v255
	v_med3_f32 v114, v166, -v255, v255
	s_bitcmp1_b32 s58, 0
	v_cvt_scalef32_pk_fp8_f32 v117, v113, v114, s93
	s_cselect_b32 s8, 0x1100, 0
	v_med3_f32 v113, v163, -v255, v255
	v_med3_f32 v114, v167, -v255, v255
	v_cmp_eq_u32_e32 vcc, 0, v181
	v_add_u32_e32 v112, s8, v191
	v_cvt_scalef32_pk_fp8_f32 v118, v113, v114, s93
	s_and_b64 vcc, exec, vcc
	s_and_b32 s37, s58, 31
	ds_write_b16 v112, v115
	ds_write_b16 v112, v116 offset:68
	ds_write_b16 v112, v117 offset:136
	ds_write_b16 v112, v118 offset:204
	s_cbranch_vccnz .LBB4_736
	s_lshl_b32 s8, s37, 7
	s_lshl_b32 s9, s58, 6
	s_and_b32 s8, s8, 0xf00
	s_and_b32 s9, s9, 64
	s_or_b32 s26, s8, s9
	s_cbranch_execnz .LBB4_730

; DI int tid_fresh(int wave) { return wave * 64 + lane_fresh(); }
; DI void attn_pass(const Frame& F, CvRide& cv, const bf16_t* __restrict__ Qb, const bf16_t* __restrict__ Kh, const bf16_t* __restrict__ Vh, char* lds, f32x16 (&o)[4], float& l_out, const int wave_s) {
;     const int tid = tid_fresh(wave_s), wid = tid >> 6, lane = tid & 63, r32 = lane & 31, hi = lane >> 5;
;     char* V_lds = lds + OFF_V; char* K_lds = lds + OFF_K;
;     float m_ref = 0.f, l_reg = 0.f; bf16x8 qr[4]; f32x16 negm = f32x16{};
; #pragma unroll
;     for (int d = 0; d < 4; ++d) o[d] = f32x16{};
;     const bf16_t* Qw = Qb + (size_t)(wid * 32 + r32) * 64 + hi * 8;
; #pragma unroll
;     for (int d0 = 0; d0 < 4; ++d0) qr[d0] = *reinterpret_cast<const bf16x8*>(Qw + d0 * 16);
;     const int sr = tid >> 4, sc = (tid & 15) * 8, vst0 = v_st(sr, sc), vst1 = v_st(32 + sr, sc);
;     const int kr = tid >> 3, kcb = (tid & 7) * 16, kst = AT_KSWZ(kr, kcb);
;     const int vb0 = (int)(uintptr_t)V_lds + v_rd_base(lane);
;     struct { bf16x8 vs0, vs1, ks0; } sr_[1];
;     const unsigned gvo = (unsigned)((sr * 128 + sc) * 2), gko = (unsigned)((kr * 64 + (tid & 7) * 8) * 2);
;     ...
;     const unsigned cv_ldo = (unsigned)(((tid >> 4) * 2 * 2048 + (tid & 15) * 4) * 4), cv_sto = (unsigned)((tid >> 3) * 2048 + 8 * (tid & 7));
;     const int cv_lw = OFF_CV + (4 * (tid & 15)) * 68 + 2 * (tid >> 4), cv_lr = OFF_CV + (tid >> 3) * 68 + 8 * (tid & 7);
;     f32x4 cvA = f32x4{}, cvB = f32x4{}; unsigned cvr0 = 0, cvr1 = 0;
;     ...
;     f32x16 pA0, pA1, pB0, pB1; float alA, alB; bf16x8 pa0, pa1, pa2, pa3; constexpr int NT = S / 64;
;     constexpr int SE = 0;
;     {
;         bf16x8 v10 = *reinterpret_cast<const bf16x8*>(&Vh[(size_t)(64 + sr) * 128 + sc]), v11 = *reinterpret_cast<const bf16x8*>(&Vh[(size_t)(96 + sr) * 128 + sc]);
;         bf16x8 k10 = *reinterpret_cast<const bf16x8*>(&Kh[(size_t)(64 + kr) * 64 + (tid & 7) * 8]);
;         AT_SLOAD(SE, 0); asm volatile("s_waitcnt vmcnt(0)" ::: "memory");
;         __syncthreads();
;         AT_SWRITE(0, SE);
;         *(bf16x8*)(V_lds + SHM_V + vst0) = v10; *(bf16x8*)(V_lds + SHM_V + vst1) = v11; *(bf16x8*)(K_lds + SHM_K + kst) = k10;
;         __syncthreads();
;     }
;     qkt(pA0, pA1, K_lds, qr, negm, r32, hi); partialSM(pA0, pA1, m_ref, negm, alA);
;     int s_prev = 0, s_cur = 1, s_next = 2;
.LBB4_764:
	v_lshlrev_b32_e32 v24, 4, v22
	v_lshlrev_b32_e32 v23, 3, v22
	v_and_b32_e32 v24, 0xc0, v24
	v_lshlrev_b32_e32 v22, 1, v22
	v_and_or_b32 v24, v23, 24, v24
	v_and_b32_e32 v22, 32, v22
	v_and_b32_e32 v23, 0x100, v23
	s_cmp_lg_u32 0, -1
	v_or3_b32 v202, v24, v22, v23
	s_cselect_b32 s2, 0, 0
	v_add_u32_e32 v192, s2, v202
	s_movk_i32 s2, 0x44
	v_lshl_or_b32 v213, v16, 14, v18
	v_mul_lo_u32 v16, v20, s2
	v_exp_f32_e32 v220, v0
	v_exp_f32_e32 v222, v1
	v_exp_f32_e32 v179, v2
	v_exp_f32_e32 v221, v3
	v_exp_f32_e32 v177, v4
	v_exp_f32_e32 v219, v5
	v_exp_f32_e32 v176, v6
	v_exp_f32_e32 v178, v7
	v_exp_f32_e32 v173, v8
	v_exp_f32_e32 v175, v9
	v_exp_f32_e32 v171, v10
	v_exp_f32_e32 v174, v11
	v_exp_f32_e32 v169, v12
	v_exp_f32_e32 v172, v13
	v_exp_f32_e32 v168, v14
	v_exp_f32_e32 v170, v15
	v_add_u32_e32 v0, 0, v21
	s_mov_b32 s2, 0x22000
	v_add3_u32 v194, v0, v16, s2
	v_add_u32_e32 v0, 0, v19
	v_mov_b32_e32 v162, v183
	v_mov_b32_e32 v163, v183
	v_mov_b32_e32 v48, v183
	v_mov_b32_e32 v49, v183
	v_lshl_or_b32 v193, v20, 11, v21
	v_add3_u32 v195, v0, v17, s2
	v_mov_b32_e32 v182, v183
	v_mov_b32_e32 v160, v183
	v_mov_b32_e32 v161, v183
	v_mov_b32_e32 v50, v183
	v_mov_b32_e32 v51, v183
	v_mov_b32_e32 v52, v183
	v_mov_b32_e32 v53, v183
	v_mov_b32_e32 v54, v183
	v_mov_b32_e32 v55, v183
	v_mov_b32_e32 v56, v183
	v_mov_b32_e32 v57, v183
	v_mov_b32_e32 v58, v183
	v_mov_b32_e32 v59, v183
	v_mov_b32_e32 v60, v183
	v_mov_b32_e32 v61, v183
	v_mov_b32_e32 v62, v183
	v_mov_b32_e32 v63, v183
	v_mov_b64_e32 v[32:33], v[48:49]
	v_mov_b64_e32 v[16:17], v[48:49]
	v_mov_b64_e32 v[0:1], v[48:49]
	v_mov_b64_e32 v[166:167], v[162:163]
	s_mov_b32 s27, 1
	s_mov_b32 s28, 0xc3e00000
	v_mov_b32_e32 v214, 0x43e00000
	s_mov_b32 s20, 0
	v_mov_b64_e32 v[34:35], v[50:51]
	v_mov_b64_e32 v[36:37], v[52:53]
	v_mov_b64_e32 v[38:39], v[54:55]
	v_mov_b64_e32 v[40:41], v[56:57]
	v_mov_b64_e32 v[42:43], v[58:59]
	v_mov_b64_e32 v[44:45], v[60:61]
	v_mov_b64_e32 v[46:47], v[62:63]
	v_mov_b64_e32 v[18:19], v[50:51]
	v_mov_b64_e32 v[20:21], v[52:53]
	v_mov_b64_e32 v[22:23], v[54:55]
	v_mov_b64_e32 v[24:25], v[56:57]
	v_mov_b64_e32 v[26:27], v[58:59]
	v_mov_b64_e32 v[28:29], v[60:61]
	v_mov_b64_e32 v[30:31], v[62:63]
	v_mov_b64_e32 v[2:3], v[50:51]
	v_mov_b64_e32 v[4:5], v[52:53]
	v_mov_b64_e32 v[6:7], v[54:55]
	v_mov_b64_e32 v[8:9], v[56:57]
	v_mov_b64_e32 v[10:11], v[58:59]
	v_mov_b64_e32 v[12:13], v[60:61]
	v_mov_b64_e32 v[14:15], v[62:63]
	v_mov_b64_e32 v[164:165], v[160:161]
	s_mov_b32 s22, 0
	s_mov_b32 s29, 1
	v_mov_b64_e32 v[184:185], v[182:183]
	v_mov_b32_e32 v81, v80
	v_mov_b32_e32 v82, v80
	v_mov_b32_e32 v83, v80
	v_mov_b32_e32 v84, v80
	v_mov_b32_e32 v85, v80
	v_mov_b32_e32 v86, v80
	v_mov_b32_e32 v87, v80
	v_mov_b32_e32 v88, v80
	v_mov_b32_e32 v89, v80
	v_mov_b32_e32 v90, v80
	v_mov_b32_e32 v91, v80
	v_mov_b32_e32 v92, v80
	v_mov_b32_e32 v93, v80
	v_mov_b32_e32 v94, v80
	v_mov_b32_e32 v95, v80
	v_mov_b32_e32 v255, 0x3f600000
	s_mov_b32 s93, 0x3b000000
	v_mbcnt_lo_u32_b32 v253, -1, 0
	v_mbcnt_hi_u32_b32 v253, -1, v253
	v_lshrrev_b32_e32 v253, 5, v253
	v_mul_u32_u24_e32 v253, 0x700, v253
	v_add_u32_e32 v253, v253, v192

; DI void finishSM(f32x16& p0, f32x16& p1, float alpha, float& l_reg, bf16x8& pa0, bf16x8& pa1, bf16x8& pa2, bf16x8& pa3) {
; #pragma unroll
;     for (int r = 0; r < 16; ++r) p1[r] = __builtin_amdgcn_exp2f(p1[r]);
;     float ps = 0;
; #pragma unroll
;     for (int r = 0; r < 16; ++r) ps += p0[r];
; #pragma unroll
;     for (int r = 0; r < 16; ++r) ps += p1[r];
;     { auto rr = __builtin_amdgcn_permlane32_swap(__float_as_uint(ps), __float_as_uint(ps), false, false); ps = __uint_as_float(rr[0]) + __uint_as_float(rr[1]); }
;     l_reg = l_reg * alpha + ps;
;     ...
;     AT_PK4(p0, 0, pa0); AT_PK4(p0, 8, pa1); AT_PK4(p1, 0, pa2); AT_PK4(p1, 8, pa3);
;     ...
; }
; DI void qkt(f32x16& p0, f32x16& p1, const char* Ks, const bf16x8* qr, const f32x16& negm, int r32, int hi) {
; #pragma unroll
;     for (int d0 = 0; d0 < 4; ++d0) { const int cb = (d0 * 16 + hi * 8) * 2;
;         const bf16x8 b0 = *reinterpret_cast<const bf16x8*>(Ks + AT_KSWZ(r32, cb));
;         const bf16x8 b1 = *reinterpret_cast<const bf16x8*>(Ks + AT_KSWZ(32 + r32, cb));
;         p0 = __builtin_amdgcn_mfma_f32_32x32x16_bf16(b0, qr[d0], d0 == 0 ? negm : p0, 0, 0, 0);
;         p1 = __builtin_amdgcn_mfma_f32_32x32x16_bf16(b1, qr[d0], d0 == 0 ? negm : p1, 0, 0, 0); }
.LBB4_775:
	s_lshl_b32 s20, s30, 13
	s_add_i32 s20, s20, 0
	v_add_u32_e32 v72, s20, v208
	v_add_u32_e32 v112, s20, v209
	v_add_u32_e32 v180, s20, v210
	s_waitcnt lgkmcnt(1)
	v_mfma_f32_32x32x16_bf16 v[128:143], v[64:67], v[156:159], v[80:95]
	ds_read_b128 v[64:67], v72 offset:49152
	ds_read_b128 v[72:75], v72 offset:53248
	ds_read_b128 v[76:79], v112 offset:49152
	ds_read_b128 v[224:227], v112 offset:53248
	v_exp_f32_e32 v182, v97
	v_exp_f32_e32 v217, v98
	v_exp_f32_e32 v218, v99
	v_exp_f32_e32 v223, v100
	v_exp_f32_e32 v232, v101
	s_waitcnt lgkmcnt(4)
	v_mfma_f32_32x32x16_bf16 v[112:127], v[68:71], v[156:159], v[80:95]
	ds_read_b128 v[68:71], v180 offset:49152
	ds_read_b128 v[228:231], v180 offset:53248
	v_exp_f32_e32 v180, v96
	v_cvt_pk_bf16_f32 v96, v220, v222
	v_cvt_pk_bf16_f32 v97, v179, v221
	v_cvt_pk_bf16_f32 v98, v177, v219
	v_cvt_pk_bf16_f32 v99, v176, v178
	s_waitcnt lgkmcnt(4)
	v_mfma_f32_32x32x16_bf16 v[112:127], v[72:75], v[152:155], v[112:127]
	v_add_f32_e32 v75, 0, v220
	v_add_f32_e32 v75, v222, v75
	v_add_f32_e32 v75, v179, v75
	v_add_f32_e32 v75, v221, v75
	v_add_f32_e32 v75, v177, v75
	v_add_f32_e32 v75, v219, v75
	v_add_f32_e32 v75, v176, v75
	v_mfma_f32_32x32x16_bf16 v[128:143], v[64:67], v[152:155], v[128:143]
	v_add_f32_e32 v75, v178, v75
	v_add_f32_e32 v75, v173, v75
	v_add_f32_e32 v75, v175, v75
	v_add_f32_e32 v75, v171, v75
	v_add_f32_e32 v75, v174, v75
	v_add_f32_e32 v75, v169, v75
	v_add_f32_e32 v75, v172, v75
	s_waitcnt lgkmcnt(3)
	v_mfma_f32_32x32x16_bf16 v[128:143], v[76:79], v[148:151], v[128:143]
	v_add_f32_e32 v75, v168, v75
	v_add_f32_e32 v75, v170, v75
	v_add_f32_e32 v75, v180, v75
	v_add_f32_e32 v75, v182, v75
	v_exp_f32_e32 v64, v102
	v_exp_f32_e32 v65, v103
	v_exp_f32_e32 v66, v104
	s_waitcnt lgkmcnt(2)
	v_mfma_f32_32x32x16_bf16 v[112:127], v[224:227], v[148:151], v[112:127]
	v_exp_f32_e32 v67, v105
	v_exp_f32_e32 v105, v106
	v_exp_f32_e32 v106, v107
	v_exp_f32_e32 v107, v108
	v_exp_f32_e32 v72, v109
	v_exp_f32_e32 v73, v110
	v_exp_f32_e32 v74, v111
	s_waitcnt lgkmcnt(1)
	v_mfma_f32_32x32x16_bf16 v[128:143], v[68:71], v[144:147], v[128:143]
	v_add_f32_e32 v68, v217, v75
	v_add_f32_e32 v68, v218, v68
	v_add_f32_e32 v68, v223, v68
	v_add_f32_e32 v68, v232, v68
	v_add_f32_e32 v68, v64, v68
	v_add_f32_e32 v68, v65, v68
	v_add_f32_e32 v68, v66, v68
	v_add_f32_e32 v68, v67, v68
	s_waitcnt lgkmcnt(0)
	v_mfma_f32_32x32x16_bf16 v[112:127], v[228:231], v[144:147], v[112:127]
	v_add_f32_e32 v68, v105, v68
	v_add_f32_e32 v68, v106, v68
	v_add_f32_e32 v68, v107, v68
	v_add_f32_e32 v68, v72, v68
	v_add_f32_e32 v68, v73, v68
	v_add_f32_e32 v215, v74, v68
	v_mov_b32_e32 v216, v215
	v_cvt_pk_bf16_f32 v108, v173, v175
	v_cvt_pk_bf16_f32 v109, v171, v174
	v_cvt_pk_bf16_f32 v110, v169, v172
	v_cvt_pk_bf16_f32 v111, v168, v170
	v_cvt_pk_bf16_f32 v100, v180, v182
	v_cvt_pk_bf16_f32 v101, v217, v218
	v_cvt_pk_bf16_f32 v102, v223, v232
	v_cvt_pk_bf16_f32 v103, v64, v65
	v_cvt_pk_bf16_f32 v104, v66, v67
	v_cvt_pk_bf16_f32 v105, v105, v106
	v_cvt_pk_bf16_f32 v106, v107, v72
	v_cvt_pk_bf16_f32 v107, v73, v74
	s_nop 1
	v_permlane32_swap_b32_e32 v215, v216
	s_add_u32 s34, s46, s16
	s_addc_u32 s35, s47, s17
	s_add_u32 s24, s34, 0x23808000
	s_addc_u32 s25, s35, 0
	s_add_u32 s66, s34, 0x2380a000
	s_addc_u32 s67, s35, 0
	s_add_u32 s37, s46, s18
	s_addc_u32 s64, s47, s19
	s_add_u32 s74, s37, 0x21884000
	s_addc_u32 s75, s64, 0
	global_load_dwordx4 v[176:179], v200, s[24:25]
	global_load_dwordx4 v[172:175], v200, s[66:67]
	global_load_dwordx4 v[168:171], v201, s[74:75]
	s_andn2_b64 vcc, exec, s[2:3]
	s_cbranch_vccnz .LBB4_777
	s_mov_b64 s[2:3], s[8:9]
	global_store_dwordx2 v193, v[184:185], s[2:3] nt
; #define AT_SBAR() __builtin_amdgcn_sched_barrier(0)
; template <int OFF> DI s16x4 tr_read(int vb) { s16x4 r; asm volatile("ds_read_b64_tr_b16 %0, %1 offset:%2" : "=&v"(r) : "v"(vb), "i"(OFF) : "memory"); return r; }
; template <int D0> DI void pv_one(f32x16& od, int vb, bf16x8 pa0, bf16x8 pa1, bf16x8 pa2, bf16x8 pa3) {
;     const s16x4 l0 = tr_read<v_rd_off(D0, 0, 0)>(vb), h0 = tr_read<v_rd_off(D0, 0, 1)>(vb), l1 = tr_read<v_rd_off(D0, 1, 0)>(vb), h1 = tr_read<v_rd_off(D0, 1, 1)>(vb);
;     const s16x4 l2 = tr_read<v_rd_off(D0, 2, 0)>(vb), h2 = tr_read<v_rd_off(D0, 2, 1)>(vb), l3 = tr_read<v_rd_off(D0, 3, 0)>(vb), h3 = tr_read<v_rd_off(D0, 3, 1)>(vb);
;     asm volatile("s_waitcnt lgkmcnt(0)" ::: "memory"); AT_SBAR();
;     ...
;     od = __builtin_amdgcn_mfma_f32_32x32x16_bf16(AT_PK(l0, h0), pa0, od, 0, 0, 0);
;     od = __builtin_amdgcn_mfma_f32_32x32x16_bf16(AT_PK(l1, h1), pa1, od, 0, 0, 0);
;     od = __builtin_amdgcn_mfma_f32_32x32x16_bf16(AT_PK(l2, h2), pa2, od, 0, 0, 0);
;     od = __builtin_amdgcn_mfma_f32_32x32x16_bf16(AT_PK(l3, h3), pa3, od, 0, 0, 0);
;     ...
; }
; DI void pv_all_sm(f32x16* o, int vb, bf16x8 pa0, bf16x8 pa1, bf16x8 pa2, bf16x8 pa3, f32x16& p0, f32x16& p1, float& m_ref, f32x16& negm, float& alpha) {
;     pv_one<0>(o[0], vb, pa0, pa1, pa2, pa3);
;     float pmax = p0[0];
; #pragma unroll
;     for (int r = 1; r < 16; ++r) pmax = fmaxf(pmax, p0[r]);
;     pv_one<1>(o[1], vb, pa0, pa1, pa2, pa3);
; #pragma unroll
;     for (int r = 0; r < 16; ++r) pmax = fmaxf(pmax, p1[r]);
;     { auto rr = __builtin_amdgcn_permlane32_swap(__float_as_uint(pmax), __float_as_uint(pmax), false, false); pmax = fmaxf(__uint_as_float(rr[0]), __uint_as_float(rr[1])); }
;     pv_one<2>(o[2], vb, pa0, pa1, pa2, pa3);
;     alpha = 1.f;
;     if (__builtin_expect(!__all(pmax <= THRL), 0)) {
;         const float dl = fmaxf(pmax, 0.f); m_ref += dl; alpha = __builtin_amdgcn_exp2f(-dl);
; #pragma unroll
;         for (int r = 0; r < 16; ++r) { p0[r] -= dl; p1[r] -= dl; }
; #pragma unroll
;         for (int r = 0; r < 16; ++r) negm[r] = -m_ref;
;     }
;     pv_one<3>(o[3], vb, pa0, pa1, pa2, pa3);
; #pragma unroll
;     for (int r = 0; r < 16; ++r) p0[r] = __builtin_amdgcn_exp2f(p0[r]);
; }
.LBB4_777:
	s_lshl_b32 s31, s29, 14
	v_add_u32_e32 v182, s31, v253
	ds_read_b64_tr_b16 v[64:65], v182 offset:0
	ds_read_b64_tr_b16 v[66:67], v182 offset:0x100
	ds_read_b64_tr_b16 v[68:69], v182 offset:0x1000
	ds_read_b64_tr_b16 v[70:71], v182 offset:0x1100
	ds_read_b64_tr_b16 v[72:73], v182 offset:0x2000
	ds_read_b64_tr_b16 v[74:75], v182 offset:0x2100
	ds_read_b64_tr_b16 v[76:77], v182 offset:0x3000
	ds_read_b64_tr_b16 v[78:79], v182 offset:0x3100
	s_waitcnt lgkmcnt(0)
	s_nop 0
	v_mfma_f32_32x32x16_bf16 v[48:63], v[64:67], v[96:99], v[48:63]
	v_max_f32_e32 v64, v128, v129
	v_max3_f32 v64, v64, v130, v131
	v_max3_f32 v64, v64, v132, v133
	v_max3_f32 v64, v64, v134, v135
	v_max3_f32 v64, v64, v136, v137
	v_mfma_f32_32x32x16_bf16 v[48:63], v[68:71], v[108:111], v[48:63]
	v_max3_f32 v64, v64, v138, v139
	v_max3_f32 v66, v64, v140, v141
	ds_read_b64_tr_b16 v[64:65], v182 offset:0x200
	v_max3_f32 v180, v66, v142, v143
	ds_read_b64_tr_b16 v[66:67], v182 offset:0x300
	ds_read_b64_tr_b16 v[68:69], v182 offset:0x1200
	ds_read_b64_tr_b16 v[70:71], v182 offset:0x1300
	v_mfma_f32_32x32x16_bf16 v[48:63], v[72:75], v[100:103], v[48:63]
	ds_read_b64_tr_b16 v[72:73], v182 offset:0x2200
	ds_read_b64_tr_b16 v[74:75], v182 offset:0x2300
	ds_read_b64_tr_b16 v[218:219], v182 offset:0x3200
	ds_read_b64_tr_b16 v[220:221], v182 offset:0x3300
	s_waitcnt lgkmcnt(0)
	v_mfma_f32_32x32x16_bf16 v[48:63], v[76:79], v[104:107], v[48:63]
	v_mfma_f32_32x32x16_bf16 v[32:47], v[64:67], v[96:99], v[32:47]
	v_max3_f32 v76, v180, v112, v113
	v_max3_f32 v64, v76, v114, v115
	ds_read_b64_tr_b16 v[66:67], v182 offset:0x400
	v_max3_f32 v64, v64, v116, v117
	v_max3_f32 v64, v64, v118, v119
	v_max3_f32 v64, v64, v120, v121
	v_max3_f32 v64, v64, v122, v123
	v_mfma_f32_32x32x16_bf16 v[32:47], v[68:71], v[108:111], v[32:47]
	ds_read_b64_tr_b16 v[68:69], v182 offset:0x500
	ds_read_b64_tr_b16 v[70:71], v182 offset:0x1400
	v_max3_f32 v64, v64, v124, v125
	v_max3_f32 v64, v64, v126, v127
	v_mov_b32_e32 v65, v64
	s_nop 1
	v_permlane32_swap_b32_e32 v64, v65
	v_mfma_f32_32x32x16_bf16 v[32:47], v[72:75], v[100:103], v[32:47]
	ds_read_b64_tr_b16 v[72:73], v182 offset:0x1500
	ds_read_b64_tr_b16 v[74:75], v182 offset:0x2400
	ds_read_b64_tr_b16 v[76:77], v182 offset:0x2500
	ds_read_b64_tr_b16 v[222:223], v182 offset:0x3400
	ds_read_b64_tr_b16 v[224:225], v182 offset:0x3500
	s_waitcnt lgkmcnt(0)
	v_mfma_f32_32x32x16_bf16 v[32:47], v[218:221], v[104:107], v[32:47]
	v_max_f32_e32 v64, v64, v65
	v_mfma_f32_32x32x16_bf16 v[16:31], v[66:69], v[96:99], v[16:31]
	v_cmp_ge_f32_e32 vcc, s26, v64
	s_cmp_eq_u64 vcc, exec
	v_mfma_f32_32x32x16_bf16 v[16:31], v[70:73], v[108:111], v[16:31]
	v_mfma_f32_32x32x16_bf16 v[16:31], v[74:77], v[100:103], v[16:31]
	v_mfma_f32_32x32x16_bf16 v[16:31], v[222:225], v[104:107], v[16:31]
	s_cbranch_scc0 .LBB4_810
	v_mov_b32_e32 v180, 1.0
.LBB4_779:
	ds_read_b64_tr_b16 v[218:219], v182 offset:0x600
	ds_read_b64_tr_b16 v[220:221], v182 offset:0x700
	ds_read_b64_tr_b16 v[222:223], v182 offset:0x1600
	ds_read_b64_tr_b16 v[224:225], v182 offset:0x1700
	ds_read_b64_tr_b16 v[226:227], v182 offset:0x2600
	ds_read_b64_tr_b16 v[228:229], v182 offset:0x2700
	ds_read_b64_tr_b16 v[230:231], v182 offset:0x3600
	ds_read_b64_tr_b16 v[232:233], v182 offset:0x3700
	s_waitcnt lgkmcnt(0)
	s_nop 0
	v_mfma_f32_32x32x16_bf16 v[0:15], v[218:221], v[96:99], v[0:15]
	s_lshl_b32 s2, s15, 14
	s_add_i32 s2, s2, 0
	s_lshl_b32 s3, s15, 13
	v_add_u32_e32 v96, s2, v203
	s_sub_i32 s65, s2, s3
	s_waitcnt vmcnt(0)
	v_add_u32_e32 v97, s2, v204
	v_mfma_f32_32x32x16_bf16 v[0:15], v[222:225], v[108:111], v[0:15]
	ds_write_b128 v96, v[176:179]
	v_add_u32_e32 v96, s65, v205
	ds_write_b128 v97, v[172:175]
	ds_write_b128 v96, v[168:171] offset:49152
	s_andn2_b64 s[2:3], exec, s[22:23]
	s_andn2_b64 vcc, exec, s[22:23]
	v_mfma_f32_32x32x16_bf16 v[0:15], v[226:229], v[100:103], v[0:15]
	v_mfma_f32_32x32x16_bf16 v[0:15], v[230:233], v[104:107], v[0:15]
	s_cbranch_vccnz .LBB4_784
	v_med3_f32 v97, v160, -v255, v255
	v_med3_f32 v98, v164, -v255, v255
	v_cvt_scalef32_pk_fp8_f32 v99, v97, v98, s93
	v_med3_f32 v97, v161, -v255, v255
	v_med3_f32 v98, v165, -v255, v255
	v_cvt_scalef32_pk_fp8_f32 v100, v97, v98, s93
	v_med3_f32 v97, v162, -v255, v255
	v_med3_f32 v98, v166, -v255, v255
	s_bitcmp1_b32 s58, 0
	v_cvt_scalef32_pk_fp8_f32 v101, v97, v98, s93
	s_cselect_b32 s8, 0x1100, 0
	v_med3_f32 v97, v163, -v255, v255
	v_med3_f32 v98, v167, -v255, v255
	v_cmp_eq_u32_e32 vcc, 0, v181
	v_add_u32_e32 v96, s8, v195
	v_cvt_scalef32_pk_fp8_f32 v102, v97, v98, s93
	s_and_b64 vcc, exec, vcc
	s_and_b32 s22, s58, 31
	ds_write_b16 v96, v99
	ds_write_b16 v96, v100 offset:68
	ds_write_b16 v96, v101 offset:136
	ds_write_b16 v96, v102 offset:204
	s_cbranch_vccnz .LBB4_808
	s_lshl_b32 s8, s22, 7
	s_lshl_b32 s9, s58, 6
	s_and_b32 s8, s8, 0xf00
	s_and_b32 s9, s9, 64
	s_or_b32 s20, s8, s9
	s_cbranch_execnz .LBB4_783

; DI void finishSM(f32x16& p0, f32x16& p1, float alpha, float& l_reg, bf16x8& pa0, bf16x8& pa1, bf16x8& pa2, bf16x8& pa3) {
; #pragma unroll
;     for (int r = 0; r < 16; ++r) p1[r] = __builtin_amdgcn_exp2f(p1[r]);
;     float ps = 0;
; #pragma unroll
;     for (int r = 0; r < 16; ++r) ps += p0[r];
; #pragma unroll
;     for (int r = 0; r < 16; ++r) ps += p1[r];
;     { auto rr = __builtin_amdgcn_permlane32_swap(__float_as_uint(ps), __float_as_uint(ps), false, false); ps = __uint_as_float(rr[0]) + __uint_as_float(rr[1]); }
;     l_reg = l_reg * alpha + ps;
;     ...
;     AT_PK4(p0, 0, pa0); AT_PK4(p0, 8, pa1); AT_PK4(p1, 0, pa2); AT_PK4(p1, 8, pa3);
;     ...
; }
; DI void qkt(f32x16& p0, f32x16& p1, const char* Ks, const bf16x8* qr, const f32x16& negm, int r32, int hi) {
; #pragma unroll
;     for (int d0 = 0; d0 < 4; ++d0) { const int cb = (d0 * 16 + hi * 8) * 2;
;         const bf16x8 b0 = *reinterpret_cast<const bf16x8*>(Ks + AT_KSWZ(r32, cb));
;         const bf16x8 b1 = *reinterpret_cast<const bf16x8*>(Ks + AT_KSWZ(32 + r32, cb));
;         p0 = __builtin_amdgcn_mfma_f32_32x32x16_bf16(b0, qr[d0], d0 == 0 ? negm : p0, 0, 0, 0);
;         p1 = __builtin_amdgcn_mfma_f32_32x32x16_bf16(b1, qr[d0], d0 == 0 ? negm : p1, 0, 0, 0); }
.LBB4_796:
	v_exp_f32_e32 v182, v128
	v_exp_f32_e32 v234, v129
	v_exp_f32_e32 v235, v130
	v_exp_f32_e32 v236, v131
	v_exp_f32_e32 v237, v132
	v_exp_f32_e32 v238, v133
	v_exp_f32_e32 v239, v134
	v_exp_f32_e32 v240, v135
	v_exp_f32_e32 v241, v136
	v_exp_f32_e32 v242, v137
	v_exp_f32_e32 v243, v138
	v_exp_f32_e32 v244, v139
	v_exp_f32_e32 v245, v140
	v_exp_f32_e32 v246, v141
	v_exp_f32_e32 v247, v142
	v_exp_f32_e32 v248, v143
	v_add_u32_e32 v101, s65, v208
	v_add_u32_e32 v102, s65, v209
	v_add_u32_e32 v103, s65, v210
	ds_read_b128 v[172:175], v101 offset:49152
	ds_read_b128 v[176:179], v101 offset:53248
	ds_read_b128 v[218:221], v102 offset:49152
	ds_read_b128 v[222:225], v102 offset:53248
	ds_read_b128 v[226:229], v103 offset:49152
	ds_read_b128 v[230:233], v103 offset:53248
	v_exp_f32_e32 v112, v112
	v_exp_f32_e32 v113, v113
	v_exp_f32_e32 v114, v114
	s_waitcnt lgkmcnt(7)
	v_mfma_f32_32x32x16_bf16 v[128:143], v[96:99], v[156:159], v[80:95]
	v_exp_f32_e32 v115, v115
	v_exp_f32_e32 v116, v116
	v_exp_f32_e32 v117, v117
	v_exp_f32_e32 v118, v118
	v_exp_f32_e32 v119, v119
	s_waitcnt lgkmcnt(6)
	v_mfma_f32_32x32x16_bf16 v[96:111], v[168:171], v[156:159], v[80:95]
	v_exp_f32_e32 v168, v120
	v_add_f32_e32 v120, 0, v182
	v_add_f32_e32 v120, v234, v120
	v_add_f32_e32 v120, v235, v120
	v_add_f32_e32 v120, v236, v120
	v_add_f32_e32 v120, v237, v120
	v_add_f32_e32 v120, v238, v120
	v_add_f32_e32 v120, v239, v120
	v_add_f32_e32 v120, v240, v120
	v_add_f32_e32 v120, v241, v120
	v_add_f32_e32 v120, v242, v120
	s_waitcnt lgkmcnt(5)
	v_mfma_f32_32x32x16_bf16 v[128:143], v[172:175], v[152:155], v[128:143]
	v_add_f32_e32 v120, v243, v120
	v_add_f32_e32 v120, v244, v120
	v_add_f32_e32 v120, v245, v120
	v_add_f32_e32 v120, v246, v120
	v_add_f32_e32 v120, v247, v120
	v_add_f32_e32 v120, v248, v120
	v_add_f32_e32 v120, v112, v120
	s_waitcnt lgkmcnt(4)
	v_mfma_f32_32x32x16_bf16 v[96:111], v[176:179], v[152:155], v[96:111]
	v_add_f32_e32 v120, v113, v120
	v_add_f32_e32 v120, v114, v120
	v_add_f32_e32 v120, v115, v120
	v_add_f32_e32 v120, v116, v120
	v_exp_f32_e32 v169, v121
	v_add_f32_e32 v120, v117, v120
	v_exp_f32_e32 v170, v122
	s_waitcnt lgkmcnt(3)
	v_mfma_f32_32x32x16_bf16 v[128:143], v[218:221], v[148:151], v[128:143]
	v_add_f32_e32 v120, v118, v120
	v_exp_f32_e32 v171, v123
	v_add_f32_e32 v120, v119, v120
	v_exp_f32_e32 v172, v124
	v_add_f32_e32 v120, v168, v120
	v_exp_f32_e32 v173, v125
	v_add_f32_e32 v120, v169, v120
	s_waitcnt lgkmcnt(2)
	v_mfma_f32_32x32x16_bf16 v[96:111], v[222:225], v[148:151], v[96:111]
	v_exp_f32_e32 v174, v126
	v_add_f32_e32 v120, v170, v120
	v_exp_f32_e32 v175, v127
	v_add_f32_e32 v120, v171, v120
	v_add_f32_e32 v120, v172, v120
	v_add_f32_e32 v120, v173, v120
	v_add_f32_e32 v120, v174, v120
	s_waitcnt lgkmcnt(1)
	v_mfma_f32_32x32x16_bf16 v[128:143], v[226:229], v[144:147], v[128:143]
	v_add_f32_e32 v217, v175, v120
	v_mov_b32_e32 v218, v217
	v_cvt_pk_bf16_f32 v120, v182, v234
	v_cvt_pk_bf16_f32 v121, v235, v236
	v_cvt_pk_bf16_f32 v122, v237, v238
	v_cvt_pk_bf16_f32 v123, v239, v240
	v_cvt_pk_bf16_f32 v124, v241, v242
	s_waitcnt lgkmcnt(0)
	v_mfma_f32_32x32x16_bf16 v[96:111], v[230:233], v[144:147], v[96:111]
	v_cvt_pk_bf16_f32 v125, v243, v244
	v_cvt_pk_bf16_f32 v126, v245, v246
	v_cvt_pk_bf16_f32 v127, v247, v248
	v_cvt_pk_bf16_f32 v112, v112, v113
	v_cvt_pk_bf16_f32 v113, v114, v115
	v_cvt_pk_bf16_f32 v114, v116, v117
	v_cvt_pk_bf16_f32 v115, v118, v119
	v_cvt_pk_bf16_f32 v116, v168, v169
	v_cvt_pk_bf16_f32 v117, v170, v171
	v_cvt_pk_bf16_f32 v118, v172, v173
	v_cvt_pk_bf16_f32 v119, v174, v175
	v_permlane32_swap_b32_e32 v217, v218
	s_add_u32 s24, s34, 0x2380c000
	s_addc_u32 s25, s35, 0
	s_add_u32 s34, s34, 0x2380e000
	s_addc_u32 s35, s35, 0
	s_add_u32 s66, s37, 0x21886000
	s_addc_u32 s67, s64, 0
	global_load_dwordx4 v[176:179], v200, s[24:25]
	global_load_dwordx4 v[172:175], v200, s[34:35]
	s_nop 0
	global_load_dwordx4 v[168:171], v201, s[66:67]
	s_and_b64 vcc, exec, s[2:3]
	s_cbranch_vccnz .LBB4_798
	s_mov_b64 s[2:3], s[8:9]
	global_store_dwordx2 v193, v[184:185], s[2:3] nt
; #define AT_SBAR() __builtin_amdgcn_sched_barrier(0)
; template <int OFF> DI s16x4 tr_read(int vb) { s16x4 r; asm volatile("ds_read_b64_tr_b16 %0, %1 offset:%2" : "=&v"(r) : "v"(vb), "i"(OFF) : "memory"); return r; }
; template <int D0> DI void pv_one(f32x16& od, int vb, bf16x8 pa0, bf16x8 pa1, bf16x8 pa2, bf16x8 pa3) {
;     const s16x4 l0 = tr_read<v_rd_off(D0, 0, 0)>(vb), h0 = tr_read<v_rd_off(D0, 0, 1)>(vb), l1 = tr_read<v_rd_off(D0, 1, 0)>(vb), h1 = tr_read<v_rd_off(D0, 1, 1)>(vb);
;     const s16x4 l2 = tr_read<v_rd_off(D0, 2, 0)>(vb), h2 = tr_read<v_rd_off(D0, 2, 1)>(vb), l3 = tr_read<v_rd_off(D0, 3, 0)>(vb), h3 = tr_read<v_rd_off(D0, 3, 1)>(vb);
;     asm volatile("s_waitcnt lgkmcnt(0)" ::: "memory"); AT_SBAR();
;     ...
;     od = __builtin_amdgcn_mfma_f32_32x32x16_bf16(AT_PK(l0, h0), pa0, od, 0, 0, 0);
;     od = __builtin_amdgcn_mfma_f32_32x32x16_bf16(AT_PK(l1, h1), pa1, od, 0, 0, 0);
;     od = __builtin_amdgcn_mfma_f32_32x32x16_bf16(AT_PK(l2, h2), pa2, od, 0, 0, 0);
;     od = __builtin_amdgcn_mfma_f32_32x32x16_bf16(AT_PK(l3, h3), pa3, od, 0, 0, 0);
;     ...
; }
; DI void pv_all_sm(f32x16* o, int vb, bf16x8 pa0, bf16x8 pa1, bf16x8 pa2, bf16x8 pa3, f32x16& p0, f32x16& p1, float& m_ref, f32x16& negm, float& alpha) {
;     pv_one<0>(o[0], vb, pa0, pa1, pa2, pa3);
;     float pmax = p0[0];
; #pragma unroll
;     for (int r = 1; r < 16; ++r) pmax = fmaxf(pmax, p0[r]);
;     pv_one<1>(o[1], vb, pa0, pa1, pa2, pa3);
; #pragma unroll
;     for (int r = 0; r < 16; ++r) pmax = fmaxf(pmax, p1[r]);
;     { auto rr = __builtin_amdgcn_permlane32_swap(__float_as_uint(pmax), __float_as_uint(pmax), false, false); pmax = fmaxf(__uint_as_float(rr[0]), __uint_as_float(rr[1])); }
;     pv_one<2>(o[2], vb, pa0, pa1, pa2, pa3);
;     alpha = 1.f;
;     if (__builtin_expect(!__all(pmax <= THRL), 0)) {
;         const float dl = fmaxf(pmax, 0.f); m_ref += dl; alpha = __builtin_amdgcn_exp2f(-dl);
; #pragma unroll
;         for (int r = 0; r < 16; ++r) { p0[r] -= dl; p1[r] -= dl; }
; #pragma unroll
;         for (int r = 0; r < 16; ++r) negm[r] = -m_ref;
;     }
;     pv_one<3>(o[3], vb, pa0, pa1, pa2, pa3);
; #pragma unroll
;     for (int r = 0; r < 16; ++r) p0[r] = __builtin_amdgcn_exp2f(p0[r]);
; }
.LBB4_798:
	v_lshl_add_u32 v219, s30, 14, v253
	ds_read_b64_tr_b16 v[220:221], v219 offset:0
	ds_read_b64_tr_b16 v[222:223], v219 offset:0x100
	ds_read_b64_tr_b16 v[224:225], v219 offset:0x1000
	ds_read_b64_tr_b16 v[226:227], v219 offset:0x1100
	ds_read_b64_tr_b16 v[228:229], v219 offset:0x2000
	ds_read_b64_tr_b16 v[230:231], v219 offset:0x2100
	ds_read_b64_tr_b16 v[232:233], v219 offset:0x3000
	ds_read_b64_tr_b16 v[234:235], v219 offset:0x3100
	s_waitcnt lgkmcnt(0)
	s_nop 0
	v_mfma_f32_32x32x16_bf16 v[48:63], v[220:223], v[120:123], v[48:63]
	v_max_f32_e32 v182, v128, v129
	ds_read_b64_tr_b16 v[220:221], v219 offset:0x200
	ds_read_b64_tr_b16 v[222:223], v219 offset:0x300
	v_max3_f32 v182, v182, v130, v131
	v_max3_f32 v182, v182, v132, v133
	v_mfma_f32_32x32x16_bf16 v[48:63], v[224:227], v[124:127], v[48:63]
	ds_read_b64_tr_b16 v[224:225], v219 offset:0x1200
	ds_read_b64_tr_b16 v[226:227], v219 offset:0x1300
	v_max3_f32 v182, v182, v134, v135
	v_max3_f32 v182, v182, v136, v137
	v_max3_f32 v182, v182, v138, v139
	v_max3_f32 v182, v182, v140, v141
	v_max3_f32 v182, v182, v142, v143
	v_mfma_f32_32x32x16_bf16 v[48:63], v[228:231], v[112:115], v[48:63]
	ds_read_b64_tr_b16 v[228:229], v219 offset:0x2200
	ds_read_b64_tr_b16 v[230:231], v219 offset:0x2300
	ds_read_b64_tr_b16 v[236:237], v219 offset:0x3200
	ds_read_b64_tr_b16 v[238:239], v219 offset:0x3300
	s_waitcnt lgkmcnt(0)
	v_mfma_f32_32x32x16_bf16 v[48:63], v[232:235], v[116:119], v[48:63]
	v_mfma_f32_32x32x16_bf16 v[32:47], v[220:223], v[120:123], v[32:47]
	v_max3_f32 v182, v182, v96, v97
	v_max3_f32 v182, v182, v98, v99
	ds_read_b64_tr_b16 v[222:223], v219 offset:0x400
	v_max3_f32 v182, v182, v100, v101
	v_max3_f32 v182, v182, v102, v103
	v_max3_f32 v182, v182, v104, v105
	v_max3_f32 v182, v182, v106, v107
	v_mfma_f32_32x32x16_bf16 v[32:47], v[224:227], v[124:127], v[32:47]
	ds_read_b64_tr_b16 v[224:225], v219 offset:0x500
	ds_read_b64_tr_b16 v[226:227], v219 offset:0x1400
	v_max3_f32 v182, v182, v108, v109
	v_max3_f32 v182, v182, v110, v111
	v_mov_b32_e32 v220, v182
	s_nop 1
	v_permlane32_swap_b32_e32 v182, v220
	v_mfma_f32_32x32x16_bf16 v[32:47], v[228:231], v[112:115], v[32:47]
	ds_read_b64_tr_b16 v[228:229], v219 offset:0x1500
	ds_read_b64_tr_b16 v[230:231], v219 offset:0x2400
	ds_read_b64_tr_b16 v[232:233], v219 offset:0x2500
	ds_read_b64_tr_b16 v[240:241], v219 offset:0x3400
	ds_read_b64_tr_b16 v[242:243], v219 offset:0x3500
	s_waitcnt lgkmcnt(0)
	v_mfma_f32_32x32x16_bf16 v[32:47], v[236:239], v[116:119], v[32:47]
	v_max_f32_e32 v220, v182, v220
	v_mfma_f32_32x32x16_bf16 v[16:31], v[222:225], v[120:123], v[16:31]
	v_cmp_ge_f32_e32 vcc, s26, v220
	s_cmp_eq_u64 vcc, exec
	v_mov_b32_e32 v182, 1.0
	v_mfma_f32_32x32x16_bf16 v[16:31], v[226:229], v[124:127], v[16:31]
	v_mfma_f32_32x32x16_bf16 v[16:31], v[230:233], v[112:115], v[16:31]
	v_mfma_f32_32x32x16_bf16 v[16:31], v[240:243], v[116:119], v[16:31]
	s_cbranch_scc0 .LBB4_811
.LBB4_799:
	ds_read_b64_tr_b16 v[220:221], v219 offset:0x600
	ds_read_b64_tr_b16 v[222:223], v219 offset:0x700
	ds_read_b64_tr_b16 v[224:225], v219 offset:0x1600
	ds_read_b64_tr_b16 v[226:227], v219 offset:0x1700
	ds_read_b64_tr_b16 v[228:229], v219 offset:0x2600
	ds_read_b64_tr_b16 v[230:231], v219 offset:0x2700
	ds_read_b64_tr_b16 v[232:233], v219 offset:0x3600
	ds_read_b64_tr_b16 v[234:235], v219 offset:0x3700
	s_waitcnt lgkmcnt(0)
	s_nop 0
	v_mfma_f32_32x32x16_bf16 v[0:15], v[220:223], v[120:123], v[0:15]
	s_add_i32 s2, s31, 0
	v_add_u32_e32 v120, s2, v203
	s_waitcnt vmcnt(0)
	ds_write_b128 v120, v[176:179]
	s_mov_b32 s20, 0
	s_andn2_b64 vcc, exec, s[22:23]
	v_mfma_f32_32x32x16_bf16 v[0:15], v[224:227], v[124:127], v[0:15]
	v_mfma_f32_32x32x16_bf16 v[0:15], v[228:231], v[112:115], v[0:15]
	v_add_u32_e32 v112, s2, v204
	ds_write_b128 v112, v[172:175]
	v_lshl_add_u32 v112, s29, 13, v206
	ds_write_b128 v112, v[168:171] offset:49152
	s_andn2_b64 s[2:3], exec, s[22:23]
	v_mfma_f32_32x32x16_bf16 v[0:15], v[232:235], v[116:119], v[0:15]
	s_cbranch_vccnz .LBB4_804
	v_med3_f32 v113, v160, -v255, v255
	v_med3_f32 v114, v164, -v255, v255
	v_cvt_scalef32_pk_fp8_f32 v115, v113, v114, s93
	v_med3_f32 v113, v161, -v255, v255
	v_med3_f32 v114, v165, -v255, v255
	v_cvt_scalef32_pk_fp8_f32 v116, v113, v114, s93
	v_med3_f32 v113, v162, -v255, v255
	v_med3_f32 v114, v166, -v255, v255
	s_bitcmp1_b32 s58, 0
	v_cvt_scalef32_pk_fp8_f32 v117, v113, v114, s93
	s_cselect_b32 s8, 0x1100, 0
	v_med3_f32 v113, v163, -v255, v255
	v_med3_f32 v114, v167, -v255, v255
	v_cmp_eq_u32_e32 vcc, 0, v181
	v_add_u32_e32 v112, s8, v195
	v_cvt_scalef32_pk_fp8_f32 v118, v113, v114, s93
	s_and_b64 vcc, exec, vcc
	s_and_b32 s24, s58, 31
	ds_write_b16 v112, v115
	ds_write_b16 v112, v116 offset:68
	ds_write_b16 v112, v117 offset:136
	ds_write_b16 v112, v118 offset:204
	s_cbranch_vccnz .LBB4_809
	s_lshl_b32 s8, s24, 7
	s_lshl_b32 s9, s58, 6
	s_and_b32 s8, s8, 0xf00
	s_and_b32 s9, s9, 64
	s_or_b32 s20, s8, s9
	s_cbranch_execnz .LBB4_803

; DI int tid_fresh(int wave) { return wave * 64 + lane_fresh(); }
; DI void attn_pass(const Frame& F, CvRide& cv, const bf16_t* __restrict__ Qb, const bf16_t* __restrict__ Kh, const bf16_t* __restrict__ Vh, char* lds, f32x16 (&o)[4], float& l_out, const int wave_s) {
;     const int tid = tid_fresh(wave_s), wid = tid >> 6, lane = tid & 63, r32 = lane & 31, hi = lane >> 5;
;     char* V_lds = lds + OFF_V; char* K_lds = lds + OFF_K;
;     float m_ref = 0.f, l_reg = 0.f; bf16x8 qr[4]; f32x16 negm = f32x16{};
; #pragma unroll
;     for (int d = 0; d < 4; ++d) o[d] = f32x16{};
;     const bf16_t* Qw = Qb + (size_t)(wid * 32 + r32) * 64 + hi * 8;
; #pragma unroll
;     for (int d0 = 0; d0 < 4; ++d0) qr[d0] = *reinterpret_cast<const bf16x8*>(Qw + d0 * 16);
;     const int sr = tid >> 4, sc = (tid & 15) * 8, vst0 = v_st(sr, sc), vst1 = v_st(32 + sr, sc);
;     const int kr = tid >> 3, kcb = (tid & 7) * 16, kst = AT_KSWZ(kr, kcb);
;     const int vb0 = (int)(uintptr_t)V_lds + v_rd_base(lane);
;     struct { bf16x8 vs0, vs1, ks0; } sr_[1];
;     const unsigned gvo = (unsigned)((sr * 128 + sc) * 2), gko = (unsigned)((kr * 64 + (tid & 7) * 8) * 2);
;     ...
;     const unsigned cv_ldo = (unsigned)(((tid >> 4) * 2 * 2048 + (tid & 15) * 4) * 4), cv_sto = (unsigned)((tid >> 3) * 2048 + 8 * (tid & 7));
;     const int cv_lw = OFF_CV + (4 * (tid & 15)) * 68 + 2 * (tid >> 4), cv_lr = OFF_CV + (tid >> 3) * 68 + 8 * (tid & 7);
;     f32x4 cvA = f32x4{}, cvB = f32x4{}; unsigned cvr0 = 0, cvr1 = 0;
;     ...
;     f32x16 pA0, pA1, pB0, pB1; float alA, alB; bf16x8 pa0, pa1, pa2, pa3; constexpr int NT = S / 64;
;     constexpr int SE = 0;
;     {
;         bf16x8 v10 = *reinterpret_cast<const bf16x8*>(&Vh[(size_t)(64 + sr) * 128 + sc]), v11 = *reinterpret_cast<const bf16x8*>(&Vh[(size_t)(96 + sr) * 128 + sc]);
;         bf16x8 k10 = *reinterpret_cast<const bf16x8*>(&Kh[(size_t)(64 + kr) * 64 + (tid & 7) * 8]);
;         AT_SLOAD(SE, 0); asm volatile("s_waitcnt vmcnt(0)" ::: "memory");
;         __syncthreads();
;         AT_SWRITE(0, SE);
;         *(bf16x8*)(V_lds + SHM_V + vst0) = v10; *(bf16x8*)(V_lds + SHM_V + vst1) = v11; *(bf16x8*)(K_lds + SHM_K + kst) = k10;
;         __syncthreads();
;     }
;     qkt(pA0, pA1, K_lds, qr, negm, r32, hi); partialSM(pA0, pA1, m_ref, negm, alA);
;     int s_prev = 0, s_cur = 1, s_next = 2;
.LBB4_838:
	v_lshlrev_b32_e32 v24, 4, v22
	v_lshlrev_b32_e32 v23, 3, v22
	v_and_b32_e32 v24, 0xc0, v24
	v_lshlrev_b32_e32 v22, 1, v22
	v_and_or_b32 v24, v23, 24, v24
	v_and_b32_e32 v22, 32, v22
	v_and_b32_e32 v23, 0x100, v23
	s_cmp_lg_u32 0, -1
	v_or3_b32 v198, v24, v22, v23
	s_cselect_b32 s2, 0, 0
	v_add_u32_e32 v191, s2, v198
	s_movk_i32 s2, 0x44
	v_lshl_or_b32 v209, v16, 14, v18
	v_mul_lo_u32 v16, v20, s2
	v_exp_f32_e32 v216, v0
	v_exp_f32_e32 v218, v1
	v_exp_f32_e32 v179, v2
	v_exp_f32_e32 v217, v3
	v_exp_f32_e32 v177, v4
	v_exp_f32_e32 v215, v5
	v_exp_f32_e32 v176, v6
	v_exp_f32_e32 v178, v7
	v_exp_f32_e32 v173, v8
	v_exp_f32_e32 v175, v9
	v_exp_f32_e32 v171, v10
	v_exp_f32_e32 v174, v11
	v_exp_f32_e32 v169, v12
	v_exp_f32_e32 v172, v13
	v_exp_f32_e32 v168, v14
	v_exp_f32_e32 v170, v15
	v_add_u32_e32 v0, 0, v21
	s_mov_b32 s2, 0x22000
	v_add3_u32 v189, v0, v16, s2
	v_add_u32_e32 v0, 0, v19
	v_mov_b32_e32 v162, v183
	v_mov_b32_e32 v163, v183
	v_mov_b32_e32 v32, v183
	v_mov_b32_e32 v33, v183
	v_mov_b32_e32 v46, v183
	v_mov_b32_e32 v47, v183
	v_lshl_or_b32 v188, v20, 11, v21
	v_add3_u32 v190, v0, v17, s2
	v_mov_b32_e32 v182, v183
	v_mov_b32_e32 v160, v183
	v_mov_b32_e32 v161, v183
	v_mov_b32_e32 v34, v183
	v_mov_b32_e32 v35, v183
	v_mov_b32_e32 v36, v183
	v_mov_b32_e32 v37, v183
	v_mov_b32_e32 v38, v183
	v_mov_b32_e32 v39, v183
	v_mov_b32_e32 v40, v183
	v_mov_b32_e32 v41, v183
	v_mov_b32_e32 v42, v183
	v_mov_b32_e32 v43, v183
	v_mov_b32_e32 v44, v183
	v_mov_b32_e32 v45, v183
	v_mov_b64_e32 v[62:63], v[46:47]
	v_mov_b64_e32 v[16:17], v[32:33]
	v_mov_b64_e32 v[0:1], v[32:33]
	v_mov_b64_e32 v[166:167], v[162:163]
	s_mov_b32 s23, 1
	s_mov_b32 s57, 2
	s_mov_b32 s56, 0xc3e00000
	v_mov_b32_e32 v210, 0x43e00000
	s_mov_b64 s[28:29], s[16:17]
	s_mov_b32 s26, 0
	v_mov_b64_e32 v[60:61], v[44:45]
	v_mov_b64_e32 v[58:59], v[42:43]
	v_mov_b64_e32 v[56:57], v[40:41]
	v_mov_b64_e32 v[54:55], v[38:39]
	v_mov_b64_e32 v[52:53], v[36:37]
	v_mov_b64_e32 v[50:51], v[34:35]
	v_mov_b64_e32 v[48:49], v[32:33]
	v_mov_b64_e32 v[18:19], v[34:35]
	v_mov_b64_e32 v[20:21], v[36:37]
	v_mov_b64_e32 v[22:23], v[38:39]
	v_mov_b64_e32 v[24:25], v[40:41]
	v_mov_b64_e32 v[26:27], v[42:43]
	v_mov_b64_e32 v[28:29], v[44:45]
	v_mov_b64_e32 v[30:31], v[46:47]
	v_mov_b64_e32 v[2:3], v[34:35]
	v_mov_b64_e32 v[4:5], v[36:37]
	v_mov_b64_e32 v[6:7], v[38:39]
	v_mov_b64_e32 v[8:9], v[40:41]
	v_mov_b64_e32 v[10:11], v[42:43]
	v_mov_b64_e32 v[12:13], v[44:45]
	v_mov_b64_e32 v[14:15], v[46:47]
	v_mov_b64_e32 v[164:165], v[160:161]
	s_mov_b32 s30, 0
	s_mov_b32 s63, 1
	v_mov_b64_e32 v[184:185], v[182:183]
	v_mov_b32_e32 v81, v80
	v_mov_b32_e32 v82, v80
	v_mov_b32_e32 v83, v80
	v_mov_b32_e32 v84, v80
	v_mov_b32_e32 v85, v80
	v_mov_b32_e32 v86, v80
	v_mov_b32_e32 v87, v80
	v_mov_b32_e32 v88, v80
	v_mov_b32_e32 v89, v80
	v_mov_b32_e32 v90, v80
	v_mov_b32_e32 v91, v80
	v_mov_b32_e32 v92, v80
	v_mov_b32_e32 v93, v80
	v_mov_b32_e32 v94, v80
	v_mov_b32_e32 v95, v80
	v_mov_b32_e32 v255, 0x3f600000
	s_mov_b32 s93, 0x3b000000
	v_mbcnt_lo_u32_b32 v253, -1, 0
	v_mbcnt_hi_u32_b32 v253, -1, v253
	v_lshrrev_b32_e32 v253, 5, v253
	v_mul_u32_u24_e32 v253, 0x700, v253
	v_add_u32_e32 v253, v253, v191

; DI void finishSM(f32x16& p0, f32x16& p1, float alpha, float& l_reg, bf16x8& pa0, bf16x8& pa1, bf16x8& pa2, bf16x8& pa3) {
; #pragma unroll
;     for (int r = 0; r < 16; ++r) p1[r] = __builtin_amdgcn_exp2f(p1[r]);
;     float ps = 0;
; #pragma unroll
;     for (int r = 0; r < 16; ++r) ps += p0[r];
; #pragma unroll
;     for (int r = 0; r < 16; ++r) ps += p1[r];
;     { auto rr = __builtin_amdgcn_permlane32_swap(__float_as_uint(ps), __float_as_uint(ps), false, false); ps = __uint_as_float(rr[0]) + __uint_as_float(rr[1]); }
;     l_reg = l_reg * alpha + ps;
;     ...
;     AT_PK4(p0, 0, pa0); AT_PK4(p0, 8, pa1); AT_PK4(p1, 0, pa2); AT_PK4(p1, 8, pa3);
;     ...
; }
; DI void qkt(f32x16& p0, f32x16& p1, const char* Ks, const bf16x8* qr, const f32x16& negm, int r32, int hi) {
; #pragma unroll
;     for (int d0 = 0; d0 < 4; ++d0) { const int cb = (d0 * 16 + hi * 8) * 2;
;         const bf16x8 b0 = *reinterpret_cast<const bf16x8*>(Ks + AT_KSWZ(r32, cb));
;         const bf16x8 b1 = *reinterpret_cast<const bf16x8*>(Ks + AT_KSWZ(32 + r32, cb));
;         p0 = __builtin_amdgcn_mfma_f32_32x32x16_bf16(b0, qr[d0], d0 == 0 ? negm : p0, 0, 0, 0);
;         p1 = __builtin_amdgcn_mfma_f32_32x32x16_bf16(b1, qr[d0], d0 == 0 ? negm : p1, 0, 0, 0); }
.LBB4_849:
	s_lshl_b32 s26, s64, 13
	s_add_i32 s26, s26, 0
	v_add_u32_e32 v72, s26, v204
	v_add_u32_e32 v112, s26, v205
	v_add_u32_e32 v180, s26, v206
	s_waitcnt lgkmcnt(1)
	v_mfma_f32_32x32x16_bf16 v[128:143], v[64:67], v[156:159], v[80:95]
	ds_read_b128 v[64:67], v72 offset:49152
	ds_read_b128 v[72:75], v72 offset:53248
	ds_read_b128 v[76:79], v112 offset:49152
	ds_read_b128 v[220:223], v112 offset:53248
	v_exp_f32_e32 v182, v97
	v_exp_f32_e32 v213, v98
	v_exp_f32_e32 v214, v99
	v_exp_f32_e32 v219, v100
	v_exp_f32_e32 v228, v101
	s_waitcnt lgkmcnt(4)
	v_mfma_f32_32x32x16_bf16 v[112:127], v[68:71], v[156:159], v[80:95]
	ds_read_b128 v[68:71], v180 offset:49152
	ds_read_b128 v[224:227], v180 offset:53248
	v_exp_f32_e32 v180, v96
	v_cvt_pk_bf16_f32 v96, v216, v218
	v_cvt_pk_bf16_f32 v97, v179, v217
	v_cvt_pk_bf16_f32 v98, v177, v215
	v_cvt_pk_bf16_f32 v99, v176, v178
	s_waitcnt lgkmcnt(4)
	v_mfma_f32_32x32x16_bf16 v[112:127], v[72:75], v[152:155], v[112:127]
	v_add_f32_e32 v75, 0, v216
	v_add_f32_e32 v75, v218, v75
	v_add_f32_e32 v75, v179, v75
	v_add_f32_e32 v75, v217, v75
	v_add_f32_e32 v75, v177, v75
	v_add_f32_e32 v75, v215, v75
	v_add_f32_e32 v75, v176, v75
	v_mfma_f32_32x32x16_bf16 v[128:143], v[64:67], v[152:155], v[128:143]
	v_add_f32_e32 v75, v178, v75
	v_add_f32_e32 v75, v173, v75
	v_add_f32_e32 v75, v175, v75
	v_add_f32_e32 v75, v171, v75
	v_add_f32_e32 v75, v174, v75
	v_add_f32_e32 v75, v169, v75
	v_add_f32_e32 v75, v172, v75
	s_waitcnt lgkmcnt(3)
	v_mfma_f32_32x32x16_bf16 v[128:143], v[76:79], v[148:151], v[128:143]
	v_add_f32_e32 v75, v168, v75
	v_add_f32_e32 v75, v170, v75
	v_add_f32_e32 v75, v180, v75
	v_add_f32_e32 v75, v182, v75
	v_exp_f32_e32 v64, v102
	v_exp_f32_e32 v65, v103
	v_exp_f32_e32 v66, v104
	s_waitcnt lgkmcnt(2)
	v_mfma_f32_32x32x16_bf16 v[112:127], v[220:223], v[148:151], v[112:127]
	v_exp_f32_e32 v67, v105
	v_exp_f32_e32 v105, v106
	v_exp_f32_e32 v106, v107
	v_exp_f32_e32 v107, v108
	v_exp_f32_e32 v72, v109
	v_exp_f32_e32 v73, v110
	v_exp_f32_e32 v74, v111
	s_waitcnt lgkmcnt(1)
	v_mfma_f32_32x32x16_bf16 v[128:143], v[68:71], v[144:147], v[128:143]
	v_add_f32_e32 v68, v213, v75
	v_add_f32_e32 v68, v214, v68
	v_add_f32_e32 v68, v219, v68
	v_add_f32_e32 v68, v228, v68
	v_add_f32_e32 v68, v64, v68
	v_add_f32_e32 v68, v65, v68
	v_add_f32_e32 v68, v66, v68
	v_add_f32_e32 v68, v67, v68
	s_waitcnt lgkmcnt(0)
	v_mfma_f32_32x32x16_bf16 v[112:127], v[224:227], v[144:147], v[112:127]
	v_add_f32_e32 v68, v105, v68
	v_add_f32_e32 v68, v106, v68
	v_add_f32_e32 v68, v107, v68
	v_add_f32_e32 v68, v72, v68
	v_add_f32_e32 v68, v73, v68
	v_add_f32_e32 v211, v74, v68
	v_mov_b32_e32 v212, v211
	v_cvt_pk_bf16_f32 v108, v173, v175
	v_cvt_pk_bf16_f32 v109, v171, v174
	v_cvt_pk_bf16_f32 v110, v169, v172
	v_cvt_pk_bf16_f32 v111, v168, v170
	v_cvt_pk_bf16_f32 v100, v180, v182
	v_cvt_pk_bf16_f32 v101, v213, v214
	v_cvt_pk_bf16_f32 v102, v219, v228
	v_cvt_pk_bf16_f32 v103, v64, v65
	v_cvt_pk_bf16_f32 v104, v66, v67
	v_cvt_pk_bf16_f32 v105, v105, v106
	v_cvt_pk_bf16_f32 v106, v107, v72
	v_cvt_pk_bf16_f32 v107, v73, v74
	s_nop 1
	v_permlane32_swap_b32_e32 v211, v212
	s_add_u32 s66, s46, s28
	s_addc_u32 s67, s47, s29
	s_add_u32 s34, s66, 0x23808000
	s_addc_u32 s35, s67, 0
	s_add_u32 s76, s66, 0x2380a000
	s_addc_u32 s77, s67, 0
	s_add_u32 s74, s46, s24
	s_addc_u32 s75, s47, s25
	s_add_u32 s78, s74, 0x21804000
	s_addc_u32 s79, s75, 0
	global_load_dwordx4 v[176:179], v196, s[34:35]
	global_load_dwordx4 v[172:175], v196, s[76:77]
	global_load_dwordx4 v[168:171], v197, s[78:79]
	s_andn2_b64 vcc, exec, s[2:3]
	s_cbranch_vccnz .LBB4_851
	s_mov_b64 s[2:3], s[8:9]
	global_store_dwordx2 v188, v[184:185], s[2:3] nt
; #define AT_SBAR() __builtin_amdgcn_sched_barrier(0)
; template <int OFF> DI s16x4 tr_read(int vb) { s16x4 r; asm volatile("ds_read_b64_tr_b16 %0, %1 offset:%2" : "=&v"(r) : "v"(vb), "i"(OFF) : "memory"); return r; }
; template <int D0> DI void pv_one(f32x16& od, int vb, bf16x8 pa0, bf16x8 pa1, bf16x8 pa2, bf16x8 pa3) {
;     const s16x4 l0 = tr_read<v_rd_off(D0, 0, 0)>(vb), h0 = tr_read<v_rd_off(D0, 0, 1)>(vb), l1 = tr_read<v_rd_off(D0, 1, 0)>(vb), h1 = tr_read<v_rd_off(D0, 1, 1)>(vb);
;     const s16x4 l2 = tr_read<v_rd_off(D0, 2, 0)>(vb), h2 = tr_read<v_rd_off(D0, 2, 1)>(vb), l3 = tr_read<v_rd_off(D0, 3, 0)>(vb), h3 = tr_read<v_rd_off(D0, 3, 1)>(vb);
;     asm volatile("s_waitcnt lgkmcnt(0)" ::: "memory"); AT_SBAR();
;     ...
;     od = __builtin_amdgcn_mfma_f32_32x32x16_bf16(AT_PK(l0, h0), pa0, od, 0, 0, 0);
;     od = __builtin_amdgcn_mfma_f32_32x32x16_bf16(AT_PK(l1, h1), pa1, od, 0, 0, 0);
;     od = __builtin_amdgcn_mfma_f32_32x32x16_bf16(AT_PK(l2, h2), pa2, od, 0, 0, 0);
;     od = __builtin_amdgcn_mfma_f32_32x32x16_bf16(AT_PK(l3, h3), pa3, od, 0, 0, 0);
;     ...
; }
; DI void pv_all_sm(f32x16* o, int vb, bf16x8 pa0, bf16x8 pa1, bf16x8 pa2, bf16x8 pa3, f32x16& p0, f32x16& p1, float& m_ref, f32x16& negm, float& alpha) {
;     pv_one<0>(o[0], vb, pa0, pa1, pa2, pa3);
;     float pmax = p0[0];
; #pragma unroll
;     for (int r = 1; r < 16; ++r) pmax = fmaxf(pmax, p0[r]);
;     pv_one<1>(o[1], vb, pa0, pa1, pa2, pa3);
; #pragma unroll
;     for (int r = 0; r < 16; ++r) pmax = fmaxf(pmax, p1[r]);
;     { auto rr = __builtin_amdgcn_permlane32_swap(__float_as_uint(pmax), __float_as_uint(pmax), false, false); pmax = fmaxf(__uint_as_float(rr[0]), __uint_as_float(rr[1])); }
;     pv_one<2>(o[2], vb, pa0, pa1, pa2, pa3);
;     alpha = 1.f;
;     if (__builtin_expect(!__all(pmax <= THRL), 0)) {
;         const float dl = fmaxf(pmax, 0.f); m_ref += dl; alpha = __builtin_amdgcn_exp2f(-dl);
; #pragma unroll
;         for (int r = 0; r < 16; ++r) { p0[r] -= dl; p1[r] -= dl; }
; #pragma unroll
;         for (int r = 0; r < 16; ++r) negm[r] = -m_ref;
;     }
;     pv_one<3>(o[3], vb, pa0, pa1, pa2, pa3);
; #pragma unroll
;     for (int r = 0; r < 16; ++r) p0[r] = __builtin_amdgcn_exp2f(p0[r]);
; }
.LBB4_851:
	s_lshl_b32 s65, s63, 14
	v_add_u32_e32 v182, s65, v253
	ds_read_b64_tr_b16 v[64:65], v182 offset:0
	ds_read_b64_tr_b16 v[66:67], v182 offset:0x100
	ds_read_b64_tr_b16 v[68:69], v182 offset:0x1000
	ds_read_b64_tr_b16 v[70:71], v182 offset:0x1100
	ds_read_b64_tr_b16 v[72:73], v182 offset:0x2000
	ds_read_b64_tr_b16 v[74:75], v182 offset:0x2100
	ds_read_b64_tr_b16 v[76:77], v182 offset:0x3000
	ds_read_b64_tr_b16 v[78:79], v182 offset:0x3100
	s_waitcnt lgkmcnt(0)
	s_nop 0
	v_mfma_f32_32x32x16_bf16 v[32:47], v[64:67], v[96:99], v[32:47]
	v_max_f32_e32 v64, v128, v129
	v_max3_f32 v64, v64, v130, v131
	v_max3_f32 v64, v64, v132, v133
	v_max3_f32 v64, v64, v134, v135
	v_max3_f32 v64, v64, v136, v137
	v_mfma_f32_32x32x16_bf16 v[32:47], v[68:71], v[108:111], v[32:47]
	v_max3_f32 v64, v64, v138, v139
	v_max3_f32 v66, v64, v140, v141
	ds_read_b64_tr_b16 v[64:65], v182 offset:0x200
	v_max3_f32 v180, v66, v142, v143
	ds_read_b64_tr_b16 v[66:67], v182 offset:0x300
	ds_read_b64_tr_b16 v[68:69], v182 offset:0x1200
	ds_read_b64_tr_b16 v[70:71], v182 offset:0x1300
	v_mfma_f32_32x32x16_bf16 v[32:47], v[72:75], v[100:103], v[32:47]
	ds_read_b64_tr_b16 v[72:73], v182 offset:0x2200
	ds_read_b64_tr_b16 v[74:75], v182 offset:0x2300
	ds_read_b64_tr_b16 v[214:215], v182 offset:0x3200
	ds_read_b64_tr_b16 v[216:217], v182 offset:0x3300
	s_waitcnt lgkmcnt(0)
	v_mfma_f32_32x32x16_bf16 v[32:47], v[76:79], v[104:107], v[32:47]
	v_mfma_f32_32x32x16_bf16 v[48:63], v[64:67], v[96:99], v[48:63]
	v_max3_f32 v76, v180, v112, v113
	v_max3_f32 v64, v76, v114, v115
	ds_read_b64_tr_b16 v[66:67], v182 offset:0x400
	v_max3_f32 v64, v64, v116, v117
	v_max3_f32 v64, v64, v118, v119
	v_max3_f32 v64, v64, v120, v121
	v_max3_f32 v64, v64, v122, v123
	v_mfma_f32_32x32x16_bf16 v[48:63], v[68:71], v[108:111], v[48:63]
	ds_read_b64_tr_b16 v[68:69], v182 offset:0x500
	ds_read_b64_tr_b16 v[70:71], v182 offset:0x1400
	v_max3_f32 v64, v64, v124, v125
	v_max3_f32 v64, v64, v126, v127
	v_mov_b32_e32 v65, v64
	s_nop 1
	v_permlane32_swap_b32_e32 v64, v65
	v_mfma_f32_32x32x16_bf16 v[48:63], v[72:75], v[100:103], v[48:63]
	ds_read_b64_tr_b16 v[72:73], v182 offset:0x1500
	ds_read_b64_tr_b16 v[74:75], v182 offset:0x2400
	ds_read_b64_tr_b16 v[76:77], v182 offset:0x2500
	ds_read_b64_tr_b16 v[218:219], v182 offset:0x3400
	ds_read_b64_tr_b16 v[220:221], v182 offset:0x3500
	s_waitcnt lgkmcnt(0)
	v_mfma_f32_32x32x16_bf16 v[48:63], v[214:217], v[104:107], v[48:63]
	v_max_f32_e32 v64, v64, v65
	v_mfma_f32_32x32x16_bf16 v[16:31], v[66:69], v[96:99], v[16:31]
	v_cmp_ge_f32_e32 vcc, s15, v64
	s_cmp_eq_u64 vcc, exec
	v_mfma_f32_32x32x16_bf16 v[16:31], v[70:73], v[108:111], v[16:31]
	v_mfma_f32_32x32x16_bf16 v[16:31], v[74:77], v[100:103], v[16:31]
	v_mfma_f32_32x32x16_bf16 v[16:31], v[218:221], v[104:107], v[16:31]
	s_cbranch_scc0 .LBB4_884
	v_mov_b32_e32 v180, 1.0
.LBB4_853:
	ds_read_b64_tr_b16 v[214:215], v182 offset:0x600
	ds_read_b64_tr_b16 v[216:217], v182 offset:0x700
	ds_read_b64_tr_b16 v[218:219], v182 offset:0x1600
	ds_read_b64_tr_b16 v[220:221], v182 offset:0x1700
	ds_read_b64_tr_b16 v[222:223], v182 offset:0x2600
	ds_read_b64_tr_b16 v[224:225], v182 offset:0x2700
	ds_read_b64_tr_b16 v[226:227], v182 offset:0x3600
	ds_read_b64_tr_b16 v[228:229], v182 offset:0x3700
	s_waitcnt lgkmcnt(0)
	s_nop 0
	v_mfma_f32_32x32x16_bf16 v[0:15], v[214:217], v[96:99], v[0:15]
	s_lshl_b32 s2, s57, 14
	s_add_i32 s2, s2, 0
	s_lshl_b32 s3, s57, 13
	v_add_u32_e32 v96, s2, v199
	s_sub_i32 s76, s2, s3
	s_waitcnt vmcnt(0)
	v_add_u32_e32 v97, s2, v200
	v_mfma_f32_32x32x16_bf16 v[0:15], v[218:221], v[108:111], v[0:15]
	ds_write_b128 v96, v[176:179]
	v_add_u32_e32 v96, s76, v201
	ds_write_b128 v97, v[172:175]
	ds_write_b128 v96, v[168:171] offset:49152
	s_andn2_b64 s[2:3], exec, s[30:31]
	s_andn2_b64 vcc, exec, s[30:31]
	v_mfma_f32_32x32x16_bf16 v[0:15], v[222:225], v[100:103], v[0:15]
	v_mfma_f32_32x32x16_bf16 v[0:15], v[226:229], v[104:107], v[0:15]
	s_cbranch_vccnz .LBB4_858
	v_med3_f32 v97, v160, -v255, v255
	v_med3_f32 v98, v164, -v255, v255
	v_cvt_scalef32_pk_fp8_f32 v99, v97, v98, s93
	v_med3_f32 v97, v161, -v255, v255
	v_med3_f32 v98, v165, -v255, v255
	v_cvt_scalef32_pk_fp8_f32 v100, v97, v98, s93
	v_med3_f32 v97, v162, -v255, v255
	v_med3_f32 v98, v166, -v255, v255
	s_bitcmp1_b32 s58, 0
	v_cvt_scalef32_pk_fp8_f32 v101, v97, v98, s93
	s_cselect_b32 s8, 0x1100, 0
	v_med3_f32 v97, v163, -v255, v255
	v_med3_f32 v98, v167, -v255, v255
	v_cmp_eq_u32_e32 vcc, 0, v181
	v_add_u32_e32 v96, s8, v190
	v_cvt_scalef32_pk_fp8_f32 v102, v97, v98, s93
	s_and_b64 vcc, exec, vcc
	s_and_b32 s30, s58, 31
	ds_write_b16 v96, v99
	ds_write_b16 v96, v100 offset:68
	ds_write_b16 v96, v101 offset:136
	ds_write_b16 v96, v102 offset:204
	s_cbranch_vccnz .LBB4_882
	s_lshl_b32 s8, s30, 7
	s_lshl_b32 s9, s58, 6
	s_and_b32 s8, s8, 0xf00
	s_and_b32 s9, s9, 64
	s_or_b32 s26, s8, s9
	s_cbranch_execnz .LBB4_857

; DI void finishSM(f32x16& p0, f32x16& p1, float alpha, float& l_reg, bf16x8& pa0, bf16x8& pa1, bf16x8& pa2, bf16x8& pa3) {
; #pragma unroll
;     for (int r = 0; r < 16; ++r) p1[r] = __builtin_amdgcn_exp2f(p1[r]);
;     float ps = 0;
; #pragma unroll
;     for (int r = 0; r < 16; ++r) ps += p0[r];
; #pragma unroll
;     for (int r = 0; r < 16; ++r) ps += p1[r];
;     { auto rr = __builtin_amdgcn_permlane32_swap(__float_as_uint(ps), __float_as_uint(ps), false, false); ps = __uint_as_float(rr[0]) + __uint_as_float(rr[1]); }
;     l_reg = l_reg * alpha + ps;
;     ...
;     AT_PK4(p0, 0, pa0); AT_PK4(p0, 8, pa1); AT_PK4(p1, 0, pa2); AT_PK4(p1, 8, pa3);
;     ...
; }
; DI void qkt(f32x16& p0, f32x16& p1, const char* Ks, const bf16x8* qr, const f32x16& negm, int r32, int hi) {
; #pragma unroll
;     for (int d0 = 0; d0 < 4; ++d0) { const int cb = (d0 * 16 + hi * 8) * 2;
;         const bf16x8 b0 = *reinterpret_cast<const bf16x8*>(Ks + AT_KSWZ(r32, cb));
;         const bf16x8 b1 = *reinterpret_cast<const bf16x8*>(Ks + AT_KSWZ(32 + r32, cb));
;         p0 = __builtin_amdgcn_mfma_f32_32x32x16_bf16(b0, qr[d0], d0 == 0 ? negm : p0, 0, 0, 0);
;         p1 = __builtin_amdgcn_mfma_f32_32x32x16_bf16(b1, qr[d0], d0 == 0 ? negm : p1, 0, 0, 0); }
.LBB4_870:
	v_exp_f32_e32 v182, v128
	v_exp_f32_e32 v230, v129
	v_exp_f32_e32 v231, v130
	v_exp_f32_e32 v232, v131
	v_exp_f32_e32 v233, v132
	v_exp_f32_e32 v234, v133
	v_exp_f32_e32 v235, v134
	v_exp_f32_e32 v236, v135
	v_exp_f32_e32 v237, v136
	v_exp_f32_e32 v238, v137
	v_exp_f32_e32 v239, v138
	v_exp_f32_e32 v240, v139
	v_exp_f32_e32 v241, v140
	v_exp_f32_e32 v242, v141
	v_exp_f32_e32 v243, v142
	v_exp_f32_e32 v244, v143
	v_add_u32_e32 v101, s76, v204
	v_add_u32_e32 v102, s76, v205
	v_add_u32_e32 v103, s76, v206
	ds_read_b128 v[172:175], v101 offset:49152
	ds_read_b128 v[176:179], v101 offset:53248
	ds_read_b128 v[214:217], v102 offset:49152
	ds_read_b128 v[218:221], v102 offset:53248
	ds_read_b128 v[222:225], v103 offset:49152
	ds_read_b128 v[226:229], v103 offset:53248
	v_exp_f32_e32 v112, v112
	v_exp_f32_e32 v113, v113
	v_exp_f32_e32 v114, v114
	s_waitcnt lgkmcnt(7)
	v_mfma_f32_32x32x16_bf16 v[128:143], v[96:99], v[156:159], v[80:95]
	v_exp_f32_e32 v115, v115
	v_exp_f32_e32 v116, v116
	v_exp_f32_e32 v117, v117
	v_exp_f32_e32 v118, v118
	v_exp_f32_e32 v119, v119
	s_waitcnt lgkmcnt(6)
	v_mfma_f32_32x32x16_bf16 v[96:111], v[168:171], v[156:159], v[80:95]
	v_exp_f32_e32 v168, v120
	v_add_f32_e32 v120, 0, v182
	v_add_f32_e32 v120, v230, v120
	v_add_f32_e32 v120, v231, v120
	v_add_f32_e32 v120, v232, v120
	v_add_f32_e32 v120, v233, v120
	v_add_f32_e32 v120, v234, v120
	v_add_f32_e32 v120, v235, v120
	v_add_f32_e32 v120, v236, v120
	v_add_f32_e32 v120, v237, v120
	v_add_f32_e32 v120, v238, v120
	s_waitcnt lgkmcnt(5)
	v_mfma_f32_32x32x16_bf16 v[128:143], v[172:175], v[152:155], v[128:143]
	v_add_f32_e32 v120, v239, v120
	v_add_f32_e32 v120, v240, v120
	v_add_f32_e32 v120, v241, v120
	v_add_f32_e32 v120, v242, v120
	v_add_f32_e32 v120, v243, v120
	v_add_f32_e32 v120, v244, v120
	v_add_f32_e32 v120, v112, v120
	s_waitcnt lgkmcnt(4)
	v_mfma_f32_32x32x16_bf16 v[96:111], v[176:179], v[152:155], v[96:111]
	v_add_f32_e32 v120, v113, v120
	v_add_f32_e32 v120, v114, v120
	v_add_f32_e32 v120, v115, v120
	v_add_f32_e32 v120, v116, v120
	v_exp_f32_e32 v169, v121
	v_add_f32_e32 v120, v117, v120
	v_exp_f32_e32 v170, v122
	s_waitcnt lgkmcnt(3)
	v_mfma_f32_32x32x16_bf16 v[128:143], v[214:217], v[148:151], v[128:143]
	v_add_f32_e32 v120, v118, v120
	v_exp_f32_e32 v171, v123
	v_add_f32_e32 v120, v119, v120
	v_exp_f32_e32 v172, v124
	v_add_f32_e32 v120, v168, v120
	v_exp_f32_e32 v173, v125
	v_add_f32_e32 v120, v169, v120
	s_waitcnt lgkmcnt(2)
	v_mfma_f32_32x32x16_bf16 v[96:111], v[218:221], v[148:151], v[96:111]
	v_exp_f32_e32 v174, v126
	v_add_f32_e32 v120, v170, v120
	v_exp_f32_e32 v175, v127
	v_add_f32_e32 v120, v171, v120
	v_add_f32_e32 v120, v172, v120
	v_add_f32_e32 v120, v173, v120
	v_add_f32_e32 v120, v174, v120
	s_waitcnt lgkmcnt(1)
	v_mfma_f32_32x32x16_bf16 v[128:143], v[222:225], v[144:147], v[128:143]
	v_add_f32_e32 v213, v175, v120
	v_mov_b32_e32 v214, v213
	v_cvt_pk_bf16_f32 v120, v182, v230
	v_cvt_pk_bf16_f32 v121, v231, v232
	v_cvt_pk_bf16_f32 v122, v233, v234
	v_cvt_pk_bf16_f32 v123, v235, v236
	v_cvt_pk_bf16_f32 v124, v237, v238
	s_waitcnt lgkmcnt(0)
	v_mfma_f32_32x32x16_bf16 v[96:111], v[226:229], v[144:147], v[96:111]
	v_cvt_pk_bf16_f32 v125, v239, v240
	v_cvt_pk_bf16_f32 v126, v241, v242
	v_cvt_pk_bf16_f32 v127, v243, v244
	v_cvt_pk_bf16_f32 v112, v112, v113
	v_cvt_pk_bf16_f32 v113, v114, v115
	v_cvt_pk_bf16_f32 v114, v116, v117
	v_cvt_pk_bf16_f32 v115, v118, v119
	v_cvt_pk_bf16_f32 v116, v168, v169
	v_cvt_pk_bf16_f32 v117, v170, v171
	v_cvt_pk_bf16_f32 v118, v172, v173
	v_cvt_pk_bf16_f32 v119, v174, v175
	v_permlane32_swap_b32_e32 v213, v214
	s_add_u32 s34, s66, 0x2380c000
	s_addc_u32 s35, s67, 0
	s_add_u32 s66, s66, 0x2380e000
	s_addc_u32 s67, s67, 0
	s_add_u32 s74, s74, 0x21806000
	s_addc_u32 s75, s75, 0
	global_load_dwordx4 v[176:179], v196, s[34:35]
	global_load_dwordx4 v[172:175], v196, s[66:67]
	s_nop 0
	global_load_dwordx4 v[168:171], v197, s[74:75]
	s_and_b64 vcc, exec, s[2:3]
	s_cbranch_vccnz .LBB4_872
	s_mov_b64 s[2:3], s[8:9]
	global_store_dwordx2 v188, v[184:185], s[2:3] nt
; #define AT_SBAR() __builtin_amdgcn_sched_barrier(0)
; template <int OFF> DI s16x4 tr_read(int vb) { s16x4 r; asm volatile("ds_read_b64_tr_b16 %0, %1 offset:%2" : "=&v"(r) : "v"(vb), "i"(OFF) : "memory"); return r; }
; template <int D0> DI void pv_one(f32x16& od, int vb, bf16x8 pa0, bf16x8 pa1, bf16x8 pa2, bf16x8 pa3) {
;     const s16x4 l0 = tr_read<v_rd_off(D0, 0, 0)>(vb), h0 = tr_read<v_rd_off(D0, 0, 1)>(vb), l1 = tr_read<v_rd_off(D0, 1, 0)>(vb), h1 = tr_read<v_rd_off(D0, 1, 1)>(vb);
;     const s16x4 l2 = tr_read<v_rd_off(D0, 2, 0)>(vb), h2 = tr_read<v_rd_off(D0, 2, 1)>(vb), l3 = tr_read<v_rd_off(D0, 3, 0)>(vb), h3 = tr_read<v_rd_off(D0, 3, 1)>(vb);
;     asm volatile("s_waitcnt lgkmcnt(0)" ::: "memory"); AT_SBAR();
;     ...
;     od = __builtin_amdgcn_mfma_f32_32x32x16_bf16(AT_PK(l0, h0), pa0, od, 0, 0, 0);
;     od = __builtin_amdgcn_mfma_f32_32x32x16_bf16(AT_PK(l1, h1), pa1, od, 0, 0, 0);
;     od = __builtin_amdgcn_mfma_f32_32x32x16_bf16(AT_PK(l2, h2), pa2, od, 0, 0, 0);
;     od = __builtin_amdgcn_mfma_f32_32x32x16_bf16(AT_PK(l3, h3), pa3, od, 0, 0, 0);
;     ...
; }
; DI void pv_all_sm(f32x16* o, int vb, bf16x8 pa0, bf16x8 pa1, bf16x8 pa2, bf16x8 pa3, f32x16& p0, f32x16& p1, float& m_ref, f32x16& negm, float& alpha) {
;     pv_one<0>(o[0], vb, pa0, pa1, pa2, pa3);
;     float pmax = p0[0];
; #pragma unroll
;     for (int r = 1; r < 16; ++r) pmax = fmaxf(pmax, p0[r]);
;     pv_one<1>(o[1], vb, pa0, pa1, pa2, pa3);
; #pragma unroll
;     for (int r = 0; r < 16; ++r) pmax = fmaxf(pmax, p1[r]);
;     { auto rr = __builtin_amdgcn_permlane32_swap(__float_as_uint(pmax), __float_as_uint(pmax), false, false); pmax = fmaxf(__uint_as_float(rr[0]), __uint_as_float(rr[1])); }
;     pv_one<2>(o[2], vb, pa0, pa1, pa2, pa3);
;     alpha = 1.f;
;     if (__builtin_expect(!__all(pmax <= THRL), 0)) {
;         const float dl = fmaxf(pmax, 0.f); m_ref += dl; alpha = __builtin_amdgcn_exp2f(-dl);
; #pragma unroll
;         for (int r = 0; r < 16; ++r) { p0[r] -= dl; p1[r] -= dl; }
; #pragma unroll
;         for (int r = 0; r < 16; ++r) negm[r] = -m_ref;
;     }
;     pv_one<3>(o[3], vb, pa0, pa1, pa2, pa3);
; #pragma unroll
;     for (int r = 0; r < 16; ++r) p0[r] = __builtin_amdgcn_exp2f(p0[r]);
; }
.LBB4_872:
	v_lshl_add_u32 v215, s64, 14, v253
	ds_read_b64_tr_b16 v[216:217], v215 offset:0
	ds_read_b64_tr_b16 v[218:219], v215 offset:0x100
	ds_read_b64_tr_b16 v[220:221], v215 offset:0x1000
	ds_read_b64_tr_b16 v[222:223], v215 offset:0x1100
	ds_read_b64_tr_b16 v[224:225], v215 offset:0x2000
	ds_read_b64_tr_b16 v[226:227], v215 offset:0x2100
	ds_read_b64_tr_b16 v[228:229], v215 offset:0x3000
	ds_read_b64_tr_b16 v[230:231], v215 offset:0x3100
	s_waitcnt lgkmcnt(0)
	s_nop 0
	v_mfma_f32_32x32x16_bf16 v[32:47], v[216:219], v[120:123], v[32:47]
	v_max_f32_e32 v182, v128, v129
	ds_read_b64_tr_b16 v[216:217], v215 offset:0x200
	ds_read_b64_tr_b16 v[218:219], v215 offset:0x300
	v_max3_f32 v182, v182, v130, v131
	v_max3_f32 v182, v182, v132, v133
	v_mfma_f32_32x32x16_bf16 v[32:47], v[220:223], v[124:127], v[32:47]
	ds_read_b64_tr_b16 v[220:221], v215 offset:0x1200
	ds_read_b64_tr_b16 v[222:223], v215 offset:0x1300
	v_max3_f32 v182, v182, v134, v135
	v_max3_f32 v182, v182, v136, v137
	v_max3_f32 v182, v182, v138, v139
	v_max3_f32 v182, v182, v140, v141
	v_max3_f32 v182, v182, v142, v143
	v_mfma_f32_32x32x16_bf16 v[32:47], v[224:227], v[112:115], v[32:47]
	ds_read_b64_tr_b16 v[224:225], v215 offset:0x2200
	ds_read_b64_tr_b16 v[226:227], v215 offset:0x2300
	ds_read_b64_tr_b16 v[232:233], v215 offset:0x3200
	ds_read_b64_tr_b16 v[234:235], v215 offset:0x3300
	s_waitcnt lgkmcnt(0)
	v_mfma_f32_32x32x16_bf16 v[32:47], v[228:231], v[116:119], v[32:47]
	v_mfma_f32_32x32x16_bf16 v[48:63], v[216:219], v[120:123], v[48:63]
	v_max3_f32 v182, v182, v96, v97
	v_max3_f32 v182, v182, v98, v99
	ds_read_b64_tr_b16 v[218:219], v215 offset:0x400
	v_max3_f32 v182, v182, v100, v101
	v_max3_f32 v182, v182, v102, v103
	v_max3_f32 v182, v182, v104, v105
	v_max3_f32 v182, v182, v106, v107
	v_mfma_f32_32x32x16_bf16 v[48:63], v[220:223], v[124:127], v[48:63]
	ds_read_b64_tr_b16 v[220:221], v215 offset:0x500
	ds_read_b64_tr_b16 v[222:223], v215 offset:0x1400
	v_max3_f32 v182, v182, v108, v109
	v_max3_f32 v182, v182, v110, v111
	v_mov_b32_e32 v216, v182
	s_nop 1
	v_permlane32_swap_b32_e32 v182, v216
	v_mfma_f32_32x32x16_bf16 v[48:63], v[224:227], v[112:115], v[48:63]
	ds_read_b64_tr_b16 v[224:225], v215 offset:0x1500
	ds_read_b64_tr_b16 v[226:227], v215 offset:0x2400
	ds_read_b64_tr_b16 v[228:229], v215 offset:0x2500
	ds_read_b64_tr_b16 v[236:237], v215 offset:0x3400
	ds_read_b64_tr_b16 v[238:239], v215 offset:0x3500
	s_waitcnt lgkmcnt(0)
	v_mfma_f32_32x32x16_bf16 v[48:63], v[232:235], v[116:119], v[48:63]
	v_max_f32_e32 v216, v182, v216
	v_mfma_f32_32x32x16_bf16 v[16:31], v[218:221], v[120:123], v[16:31]
	v_cmp_ge_f32_e32 vcc, s15, v216
	s_cmp_eq_u64 vcc, exec
	v_mov_b32_e32 v182, 1.0
	v_mfma_f32_32x32x16_bf16 v[16:31], v[222:225], v[124:127], v[16:31]
	v_mfma_f32_32x32x16_bf16 v[16:31], v[226:229], v[112:115], v[16:31]
	v_mfma_f32_32x32x16_bf16 v[16:31], v[236:239], v[116:119], v[16:31]
	s_cbranch_scc0 .LBB4_885
.LBB4_873:
	ds_read_b64_tr_b16 v[216:217], v215 offset:0x600
	ds_read_b64_tr_b16 v[218:219], v215 offset:0x700
	ds_read_b64_tr_b16 v[220:221], v215 offset:0x1600
	ds_read_b64_tr_b16 v[222:223], v215 offset:0x1700
	ds_read_b64_tr_b16 v[224:225], v215 offset:0x2600
	ds_read_b64_tr_b16 v[226:227], v215 offset:0x2700
	ds_read_b64_tr_b16 v[228:229], v215 offset:0x3600
	ds_read_b64_tr_b16 v[230:231], v215 offset:0x3700
	s_waitcnt lgkmcnt(0)
	s_nop 0
	v_mfma_f32_32x32x16_bf16 v[0:15], v[216:219], v[120:123], v[0:15]
	s_add_i32 s2, s65, 0
	v_add_u32_e32 v120, s2, v199
	s_waitcnt vmcnt(0)
	ds_write_b128 v120, v[176:179]
	s_mov_b32 s26, 0
	s_andn2_b64 vcc, exec, s[30:31]
	v_mfma_f32_32x32x16_bf16 v[0:15], v[220:223], v[124:127], v[0:15]
	v_mfma_f32_32x32x16_bf16 v[0:15], v[224:227], v[112:115], v[0:15]
	v_add_u32_e32 v112, s2, v200
	ds_write_b128 v112, v[172:175]
	v_lshl_add_u32 v112, s63, 13, v202
	ds_write_b128 v112, v[168:171] offset:49152
	s_andn2_b64 s[2:3], exec, s[30:31]
	v_mfma_f32_32x32x16_bf16 v[0:15], v[228:231], v[116:119], v[0:15]
	s_cbranch_vccnz .LBB4_878
	v_med3_f32 v113, v160, -v255, v255
	v_med3_f32 v114, v164, -v255, v255
	v_cvt_scalef32_pk_fp8_f32 v115, v113, v114, s93
	v_med3_f32 v113, v161, -v255, v255
	v_med3_f32 v114, v165, -v255, v255
	v_cvt_scalef32_pk_fp8_f32 v116, v113, v114, s93
	v_med3_f32 v113, v162, -v255, v255
	v_med3_f32 v114, v166, -v255, v255
	s_bitcmp1_b32 s58, 0
	v_cvt_scalef32_pk_fp8_f32 v117, v113, v114, s93
	s_cselect_b32 s8, 0x1100, 0
	v_med3_f32 v113, v163, -v255, v255
	v_med3_f32 v114, v167, -v255, v255
	v_cmp_eq_u32_e32 vcc, 0, v181
	v_add_u32_e32 v112, s8, v190
	v_cvt_scalef32_pk_fp8_f32 v118, v113, v114, s93
	s_and_b64 vcc, exec, vcc
	s_and_b32 s34, s58, 31
	ds_write_b16 v112, v115
	ds_write_b16 v112, v116 offset:68
	ds_write_b16 v112, v117 offset:136
	ds_write_b16 v112, v118 offset:204
	s_cbranch_vccnz .LBB4_883
	s_lshl_b32 s8, s34, 7
	s_lshl_b32 s9, s58, 6
	s_and_b32 s8, s8, 0xf00
	s_and_b32 s9, s9, 64
	s_or_b32 s26, s8, s9
	s_cbranch_execnz .LBB4_877

; DI int tid_fresh(int wave) { return wave * 64 + lane_fresh(); }
; DI void attn_pass(const Frame& F, CvRide& cv, const bf16_t* __restrict__ Qb, const bf16_t* __restrict__ Kh, const bf16_t* __restrict__ Vh, char* lds, f32x16 (&o)[4], float& l_out, const int wave_s) {
;     const int tid = tid_fresh(wave_s), wid = tid >> 6, lane = tid & 63, r32 = lane & 31, hi = lane >> 5;
;     char* V_lds = lds + OFF_V; char* K_lds = lds + OFF_K;
;     float m_ref = 0.f, l_reg = 0.f; bf16x8 qr[4]; f32x16 negm = f32x16{};
; #pragma unroll
;     for (int d = 0; d < 4; ++d) o[d] = f32x16{};
;     const bf16_t* Qw = Qb + (size_t)(wid * 32 + r32) * 64 + hi * 8;
; #pragma unroll
;     for (int d0 = 0; d0 < 4; ++d0) qr[d0] = *reinterpret_cast<const bf16x8*>(Qw + d0 * 16);
;     const int sr = tid >> 4, sc = (tid & 15) * 8, vst0 = v_st(sr, sc), vst1 = v_st(32 + sr, sc);
;     const int kr = tid >> 3, kcb = (tid & 7) * 16, kst = AT_KSWZ(kr, kcb);
;     const int vb0 = (int)(uintptr_t)V_lds + v_rd_base(lane);
;     struct { bf16x8 vs0, vs1, ks0; } sr_[1];
;     const unsigned gvo = (unsigned)((sr * 128 + sc) * 2), gko = (unsigned)((kr * 64 + (tid & 7) * 8) * 2);
;     ...
;     const unsigned cv_ldo = (unsigned)(((tid >> 4) * 2 * 2048 + (tid & 15) * 4) * 4), cv_sto = (unsigned)((tid >> 3) * 2048 + 8 * (tid & 7));
;     const int cv_lw = OFF_CV + (4 * (tid & 15)) * 68 + 2 * (tid >> 4), cv_lr = OFF_CV + (tid >> 3) * 68 + 8 * (tid & 7);
;     f32x4 cvA = f32x4{}, cvB = f32x4{}; unsigned cvr0 = 0, cvr1 = 0;
;     ...
;     f32x16 pA0, pA1, pB0, pB1; float alA, alB; bf16x8 pa0, pa1, pa2, pa3; constexpr int NT = S / 64;
;     constexpr int SE = 0;
;     {
;         bf16x8 v10 = *reinterpret_cast<const bf16x8*>(&Vh[(size_t)(64 + sr) * 128 + sc]), v11 = *reinterpret_cast<const bf16x8*>(&Vh[(size_t)(96 + sr) * 128 + sc]);
;         bf16x8 k10 = *reinterpret_cast<const bf16x8*>(&Kh[(size_t)(64 + kr) * 64 + (tid & 7) * 8]);
;         AT_SLOAD(SE, 0); asm volatile("s_waitcnt vmcnt(0)" ::: "memory");
;         __syncthreads();
;         AT_SWRITE(0, SE);
;         *(bf16x8*)(V_lds + SHM_V + vst0) = v10; *(bf16x8*)(V_lds + SHM_V + vst1) = v11; *(bf16x8*)(K_lds + SHM_K + kst) = k10;
;         __syncthreads();
;     }
;     qkt(pA0, pA1, K_lds, qr, negm, r32, hi); partialSM(pA0, pA1, m_ref, negm, alA);
;     int s_prev = 0, s_cur = 1, s_next = 2;
.LBB4_912:
	v_lshlrev_b32_e32 v24, 4, v22
	v_lshlrev_b32_e32 v23, 3, v22
	v_and_b32_e32 v24, 0xc0, v24
	v_lshlrev_b32_e32 v22, 1, v22
	v_and_or_b32 v24, v23, 24, v24
	v_and_b32_e32 v22, 32, v22
	v_and_b32_e32 v23, 0x100, v23
	s_cmp_lg_u32 0, -1
	v_or3_b32 v202, v24, v22, v23
	s_cselect_b32 s2, 0, 0
	v_add_u32_e32 v192, s2, v202
	s_movk_i32 s2, 0x44
	v_lshl_or_b32 v213, v16, 14, v18
	v_mul_lo_u32 v16, v20, s2
	v_exp_f32_e32 v220, v0
	v_add_u32_e32 v0, 0, v21
	s_mov_b32 s2, 0x22000
	v_add3_u32 v194, v0, v16, s2
	v_add_u32_e32 v0, 0, v19
	v_add3_u32 v195, v0, v17, s2
	s_and_b32 s2, s33, 7
	s_lshl_b32 s2, s2, 2
	s_lshl_b32 s3, s60, 1
	v_exp_f32_e32 v222, v1
	v_exp_f32_e32 v179, v2
	v_exp_f32_e32 v221, v3
	v_exp_f32_e32 v177, v4
	v_exp_f32_e32 v219, v5
	v_exp_f32_e32 v176, v6
	v_exp_f32_e32 v178, v7
	v_exp_f32_e32 v173, v8
	v_exp_f32_e32 v175, v9
	v_exp_f32_e32 v171, v10
	v_exp_f32_e32 v174, v11
	v_exp_f32_e32 v169, v12
	v_exp_f32_e32 v172, v13
	v_exp_f32_e32 v168, v14
	v_exp_f32_e32 v170, v15
	s_add_i32 s2, s2, s3
	s_add_i32 s2, s2, 32
	v_mov_b32_e32 v162, v183
	v_mov_b32_e32 v163, v183
	v_mov_b32_e32 v48, v183
	v_mov_b32_e32 v49, v183
	v_lshl_or_b32 v193, v20, 11, v21
	s_ashr_i32 s3, s2, 31
	v_mov_b32_e32 v182, v183
	v_mov_b32_e32 v160, v183
	v_mov_b32_e32 v161, v183
	v_mov_b32_e32 v50, v183
	v_mov_b32_e32 v51, v183
	v_mov_b32_e32 v52, v183
	v_mov_b32_e32 v53, v183
	v_mov_b32_e32 v54, v183
	v_mov_b32_e32 v55, v183
	v_mov_b32_e32 v56, v183
	v_mov_b32_e32 v57, v183
	v_mov_b32_e32 v58, v183
	v_mov_b32_e32 v59, v183
	v_mov_b32_e32 v60, v183
	v_mov_b32_e32 v61, v183
	v_mov_b32_e32 v62, v183
	v_mov_b32_e32 v63, v183
	v_mov_b64_e32 v[32:33], v[48:49]
	v_mov_b64_e32 v[16:17], v[48:49]
	v_mov_b64_e32 v[0:1], v[48:49]
	v_mov_b64_e32 v[166:167], v[162:163]
	s_mov_b32 s27, 1
	s_lshl_b64 s[20:21], s[2:3], 19
	s_mov_b32 s28, 0xc3e00000
	v_mov_b32_e32 v214, 0x43e00000
	s_mov_b32 s18, 0
	v_mov_b64_e32 v[34:35], v[50:51]
	v_mov_b64_e32 v[36:37], v[52:53]
	v_mov_b64_e32 v[38:39], v[54:55]
	v_mov_b64_e32 v[40:41], v[56:57]
	v_mov_b64_e32 v[42:43], v[58:59]
	v_mov_b64_e32 v[44:45], v[60:61]
	v_mov_b64_e32 v[46:47], v[62:63]
	v_mov_b64_e32 v[18:19], v[50:51]
	v_mov_b64_e32 v[20:21], v[52:53]
	v_mov_b64_e32 v[22:23], v[54:55]
	v_mov_b64_e32 v[24:25], v[56:57]
	v_mov_b64_e32 v[26:27], v[58:59]
	v_mov_b64_e32 v[28:29], v[60:61]
	v_mov_b64_e32 v[30:31], v[62:63]
	v_mov_b64_e32 v[2:3], v[50:51]
	v_mov_b64_e32 v[4:5], v[52:53]
	v_mov_b64_e32 v[6:7], v[54:55]
	v_mov_b64_e32 v[8:9], v[56:57]
	v_mov_b64_e32 v[10:11], v[58:59]
	v_mov_b64_e32 v[12:13], v[60:61]
	v_mov_b64_e32 v[14:15], v[62:63]
	v_mov_b64_e32 v[164:165], v[160:161]
	s_mov_b32 s22, 0
	s_mov_b32 s29, 1
	v_mov_b64_e32 v[184:185], v[182:183]
	v_mov_b32_e32 v81, v80
	v_mov_b32_e32 v82, v80
	v_mov_b32_e32 v83, v80
	v_mov_b32_e32 v84, v80
	v_mov_b32_e32 v85, v80
	v_mov_b32_e32 v86, v80
	v_mov_b32_e32 v87, v80
	v_mov_b32_e32 v88, v80
	v_mov_b32_e32 v89, v80
	v_mov_b32_e32 v90, v80
	v_mov_b32_e32 v91, v80
	v_mov_b32_e32 v92, v80
	v_mov_b32_e32 v93, v80
	v_mov_b32_e32 v94, v80
	v_mov_b32_e32 v95, v80
	v_mov_b32_e32 v255, 0x3f600000
	s_mov_b32 s93, 0x3b000000
	v_mbcnt_lo_u32_b32 v253, -1, 0
	v_mbcnt_hi_u32_b32 v253, -1, v253
	v_lshrrev_b32_e32 v253, 5, v253
	v_mul_u32_u24_e32 v253, 0x700, v253
	v_add_u32_e32 v253, v253, v192

; DI void finishSM(f32x16& p0, f32x16& p1, float alpha, float& l_reg, bf16x8& pa0, bf16x8& pa1, bf16x8& pa2, bf16x8& pa3) {
; #pragma unroll
;     for (int r = 0; r < 16; ++r) p1[r] = __builtin_amdgcn_exp2f(p1[r]);
;     float ps = 0;
; #pragma unroll
;     for (int r = 0; r < 16; ++r) ps += p0[r];
; #pragma unroll
;     for (int r = 0; r < 16; ++r) ps += p1[r];
;     { auto rr = __builtin_amdgcn_permlane32_swap(__float_as_uint(ps), __float_as_uint(ps), false, false); ps = __uint_as_float(rr[0]) + __uint_as_float(rr[1]); }
;     l_reg = l_reg * alpha + ps;
;     ...
;     AT_PK4(p0, 0, pa0); AT_PK4(p0, 8, pa1); AT_PK4(p1, 0, pa2); AT_PK4(p1, 8, pa3);
;     ...
; }
; DI void qkt(f32x16& p0, f32x16& p1, const char* Ks, const bf16x8* qr, const f32x16& negm, int r32, int hi) {
; #pragma unroll
;     for (int d0 = 0; d0 < 4; ++d0) { const int cb = (d0 * 16 + hi * 8) * 2;
;         const bf16x8 b0 = *reinterpret_cast<const bf16x8*>(Ks + AT_KSWZ(r32, cb));
;         const bf16x8 b1 = *reinterpret_cast<const bf16x8*>(Ks + AT_KSWZ(32 + r32, cb));
;         p0 = __builtin_amdgcn_mfma_f32_32x32x16_bf16(b0, qr[d0], d0 == 0 ? negm : p0, 0, 0, 0);
;         p1 = __builtin_amdgcn_mfma_f32_32x32x16_bf16(b1, qr[d0], d0 == 0 ? negm : p1, 0, 0, 0); }
.LBB4_923:
	s_lshl_b32 s18, s30, 13
	s_add_i32 s18, s18, 0
	v_add_u32_e32 v72, s18, v208
	v_add_u32_e32 v112, s18, v209
	v_add_u32_e32 v180, s18, v210
	s_waitcnt lgkmcnt(1)
	v_mfma_f32_32x32x16_bf16 v[128:143], v[64:67], v[156:159], v[80:95]
	ds_read_b128 v[64:67], v72 offset:49152
	ds_read_b128 v[72:75], v72 offset:53248
	ds_read_b128 v[76:79], v112 offset:49152
	ds_read_b128 v[224:227], v112 offset:53248
	v_exp_f32_e32 v182, v97
	v_exp_f32_e32 v217, v98
	v_exp_f32_e32 v218, v99
	v_exp_f32_e32 v223, v100
	v_exp_f32_e32 v232, v101
	s_waitcnt lgkmcnt(4)
	v_mfma_f32_32x32x16_bf16 v[112:127], v[68:71], v[156:159], v[80:95]
	ds_read_b128 v[68:71], v180 offset:49152
	ds_read_b128 v[228:231], v180 offset:53248
	v_exp_f32_e32 v180, v96
	v_cvt_pk_bf16_f32 v96, v220, v222
	v_cvt_pk_bf16_f32 v97, v179, v221
	v_cvt_pk_bf16_f32 v98, v177, v219
	v_cvt_pk_bf16_f32 v99, v176, v178
	s_waitcnt lgkmcnt(4)
	v_mfma_f32_32x32x16_bf16 v[112:127], v[72:75], v[152:155], v[112:127]
	v_add_f32_e32 v75, 0, v220
	v_add_f32_e32 v75, v222, v75
	v_add_f32_e32 v75, v179, v75
	v_add_f32_e32 v75, v221, v75
	v_add_f32_e32 v75, v177, v75
	v_add_f32_e32 v75, v219, v75
	v_add_f32_e32 v75, v176, v75
	v_mfma_f32_32x32x16_bf16 v[128:143], v[64:67], v[152:155], v[128:143]
	v_add_f32_e32 v75, v178, v75
	v_add_f32_e32 v75, v173, v75
	v_add_f32_e32 v75, v175, v75
	v_add_f32_e32 v75, v171, v75
	v_add_f32_e32 v75, v174, v75
	v_add_f32_e32 v75, v169, v75
	v_add_f32_e32 v75, v172, v75
	s_waitcnt lgkmcnt(3)
	v_mfma_f32_32x32x16_bf16 v[128:143], v[76:79], v[148:151], v[128:143]
	v_add_f32_e32 v75, v168, v75
	v_add_f32_e32 v75, v170, v75
	v_add_f32_e32 v75, v180, v75
	v_add_f32_e32 v75, v182, v75
	v_exp_f32_e32 v64, v102
	v_exp_f32_e32 v65, v103
	v_exp_f32_e32 v66, v104
	s_waitcnt lgkmcnt(2)
	v_mfma_f32_32x32x16_bf16 v[112:127], v[224:227], v[148:151], v[112:127]
	v_exp_f32_e32 v67, v105
	v_exp_f32_e32 v105, v106
	v_exp_f32_e32 v106, v107
	v_exp_f32_e32 v107, v108
	v_exp_f32_e32 v72, v109
	v_exp_f32_e32 v73, v110
	v_exp_f32_e32 v74, v111
	s_waitcnt lgkmcnt(1)
	v_mfma_f32_32x32x16_bf16 v[128:143], v[68:71], v[144:147], v[128:143]
	v_add_f32_e32 v68, v217, v75
	v_add_f32_e32 v68, v218, v68
	v_add_f32_e32 v68, v223, v68
	v_add_f32_e32 v68, v232, v68
	v_add_f32_e32 v68, v64, v68
	v_add_f32_e32 v68, v65, v68
	v_add_f32_e32 v68, v66, v68
	v_add_f32_e32 v68, v67, v68
	s_waitcnt lgkmcnt(0)
	v_mfma_f32_32x32x16_bf16 v[112:127], v[228:231], v[144:147], v[112:127]
	v_add_f32_e32 v68, v105, v68
	v_add_f32_e32 v68, v106, v68
	v_add_f32_e32 v68, v107, v68
	v_add_f32_e32 v68, v72, v68
	v_add_f32_e32 v68, v73, v68
	v_add_f32_e32 v215, v74, v68
	v_mov_b32_e32 v216, v215
	v_cvt_pk_bf16_f32 v108, v173, v175
	v_cvt_pk_bf16_f32 v109, v171, v174
	v_cvt_pk_bf16_f32 v110, v169, v172
	v_cvt_pk_bf16_f32 v111, v168, v170
	v_cvt_pk_bf16_f32 v100, v180, v182
	v_cvt_pk_bf16_f32 v101, v217, v218
	v_cvt_pk_bf16_f32 v102, v223, v232
	v_cvt_pk_bf16_f32 v103, v64, v65
	v_cvt_pk_bf16_f32 v104, v66, v67
	v_cvt_pk_bf16_f32 v105, v105, v106
	v_cvt_pk_bf16_f32 v106, v107, v72
	v_cvt_pk_bf16_f32 v107, v73, v74
	s_nop 1
	v_permlane32_swap_b32_e32 v215, v216
	s_add_u32 s34, s46, s16
	s_addc_u32 s35, s47, s17
	s_add_u32 s24, s34, 0x23808000
	s_addc_u32 s25, s35, 0
	s_add_u32 s54, s34, 0x2380a000
	s_addc_u32 s55, s35, 0
	s_add_u32 s42, s46, s20
	s_addc_u32 s43, s47, s21
	s_add_u32 s56, s42, 0x21884000
	s_addc_u32 s57, s43, 0
	global_load_dwordx4 v[176:179], v200, s[24:25]
	global_load_dwordx4 v[172:175], v200, s[54:55]
	global_load_dwordx4 v[168:171], v201, s[56:57]
	s_andn2_b64 vcc, exec, s[2:3]
	s_cbranch_vccnz .LBB4_925
	s_mov_b64 s[2:3], s[8:9]
	global_store_dwordx2 v193, v[184:185], s[2:3] nt

; #define AT_SBAR() __builtin_amdgcn_sched_barrier(0)
; template <int OFF> DI s16x4 tr_read(int vb) { s16x4 r; asm volatile("ds_read_b64_tr_b16 %0, %1 offset:%2" : "=&v"(r) : "v"(vb), "i"(OFF) : "memory"); return r; }
; template <int D0> DI void pv_one(f32x16& od, int vb, bf16x8 pa0, bf16x8 pa1, bf16x8 pa2, bf16x8 pa3) {
;     const s16x4 l0 = tr_read<v_rd_off(D0, 0, 0)>(vb), h0 = tr_read<v_rd_off(D0, 0, 1)>(vb), l1 = tr_read<v_rd_off(D0, 1, 0)>(vb), h1 = tr_read<v_rd_off(D0, 1, 1)>(vb);
;     const s16x4 l2 = tr_read<v_rd_off(D0, 2, 0)>(vb), h2 = tr_read<v_rd_off(D0, 2, 1)>(vb), l3 = tr_read<v_rd_off(D0, 3, 0)>(vb), h3 = tr_read<v_rd_off(D0, 3, 1)>(vb);
;     asm volatile("s_waitcnt lgkmcnt(0)" ::: "memory"); AT_SBAR();
;     ...
;     od = __builtin_amdgcn_mfma_f32_32x32x16_bf16(AT_PK(l0, h0), pa0, od, 0, 0, 0);
;     od = __builtin_amdgcn_mfma_f32_32x32x16_bf16(AT_PK(l1, h1), pa1, od, 0, 0, 0);
;     od = __builtin_amdgcn_mfma_f32_32x32x16_bf16(AT_PK(l2, h2), pa2, od, 0, 0, 0);
;     od = __builtin_amdgcn_mfma_f32_32x32x16_bf16(AT_PK(l3, h3), pa3, od, 0, 0, 0);
.LBB4_927:
	ds_read_b64_tr_b16 v[218:219], v182 offset:0x600
	ds_read_b64_tr_b16 v[220:221], v182 offset:0x700
	ds_read_b64_tr_b16 v[222:223], v182 offset:0x1600
	ds_read_b64_tr_b16 v[224:225], v182 offset:0x1700
	ds_read_b64_tr_b16 v[226:227], v182 offset:0x2600
	ds_read_b64_tr_b16 v[228:229], v182 offset:0x2700
	ds_read_b64_tr_b16 v[230:231], v182 offset:0x3600
	ds_read_b64_tr_b16 v[232:233], v182 offset:0x3700
	s_waitcnt lgkmcnt(0)
	s_nop 0
	v_mfma_f32_32x32x16_bf16 v[0:15], v[218:221], v[96:99], v[0:15]
	s_lshl_b32 s2, s15, 14
	s_add_i32 s2, s2, 0
	s_lshl_b32 s3, s15, 13
	v_add_u32_e32 v96, s2, v203
	s_sub_i32 s54, s2, s3
	s_waitcnt vmcnt(0)
	v_add_u32_e32 v97, s2, v204
	v_mfma_f32_32x32x16_bf16 v[0:15], v[222:225], v[108:111], v[0:15]
	ds_write_b128 v96, v[176:179]
	v_add_u32_e32 v96, s54, v205
	ds_write_b128 v97, v[172:175]
	ds_write_b128 v96, v[168:171] offset:49152
	s_andn2_b64 s[2:3], exec, s[22:23]
	s_andn2_b64 vcc, exec, s[22:23]
	v_mfma_f32_32x32x16_bf16 v[0:15], v[226:229], v[100:103], v[0:15]
	v_mfma_f32_32x32x16_bf16 v[0:15], v[230:233], v[104:107], v[0:15]
	s_cbranch_vccnz .LBB4_932
	v_med3_f32 v97, v160, -v255, v255
	v_med3_f32 v98, v164, -v255, v255
	v_cvt_scalef32_pk_fp8_f32 v99, v97, v98, s93
	v_med3_f32 v97, v161, -v255, v255
	v_med3_f32 v98, v165, -v255, v255
	v_cvt_scalef32_pk_fp8_f32 v100, v97, v98, s93
	v_med3_f32 v97, v162, -v255, v255
	v_med3_f32 v98, v166, -v255, v255
	s_bitcmp1_b32 s58, 0
	v_cvt_scalef32_pk_fp8_f32 v101, v97, v98, s93
	s_cselect_b32 s8, 0x1100, 0
	v_med3_f32 v97, v163, -v255, v255
	v_med3_f32 v98, v167, -v255, v255
	v_cmp_eq_u32_e32 vcc, 0, v181
	v_add_u32_e32 v96, s8, v195
	v_cvt_scalef32_pk_fp8_f32 v102, v97, v98, s93
	s_and_b64 vcc, exec, vcc
	s_and_b32 s22, s58, 31
	ds_write_b16 v96, v99
	ds_write_b16 v96, v100 offset:68
	ds_write_b16 v96, v101 offset:136
	ds_write_b16 v96, v102 offset:204
	s_cbranch_vccnz .LBB4_956
	s_lshl_b32 s8, s22, 7
	s_lshl_b32 s9, s58, 6
	s_and_b32 s8, s8, 0xf00
	s_and_b32 s9, s9, 64
	s_or_b32 s18, s8, s9
	s_cbranch_execnz .LBB4_931

; DI void finishSM(f32x16& p0, f32x16& p1, float alpha, float& l_reg, bf16x8& pa0, bf16x8& pa1, bf16x8& pa2, bf16x8& pa3) {
; #pragma unroll
;     for (int r = 0; r < 16; ++r) p1[r] = __builtin_amdgcn_exp2f(p1[r]);
;     float ps = 0;
; #pragma unroll
;     for (int r = 0; r < 16; ++r) ps += p0[r];
; #pragma unroll
;     for (int r = 0; r < 16; ++r) ps += p1[r];
;     { auto rr = __builtin_amdgcn_permlane32_swap(__float_as_uint(ps), __float_as_uint(ps), false, false); ps = __uint_as_float(rr[0]) + __uint_as_float(rr[1]); }
;     l_reg = l_reg * alpha + ps;
;     ...
;     AT_PK4(p0, 0, pa0); AT_PK4(p0, 8, pa1); AT_PK4(p1, 0, pa2); AT_PK4(p1, 8, pa3);
;     ...
; }
; DI void qkt(f32x16& p0, f32x16& p1, const char* Ks, const bf16x8* qr, const f32x16& negm, int r32, int hi) {
; #pragma unroll
;     for (int d0 = 0; d0 < 4; ++d0) { const int cb = (d0 * 16 + hi * 8) * 2;
;         const bf16x8 b0 = *reinterpret_cast<const bf16x8*>(Ks + AT_KSWZ(r32, cb));
;         const bf16x8 b1 = *reinterpret_cast<const bf16x8*>(Ks + AT_KSWZ(32 + r32, cb));
;         p0 = __builtin_amdgcn_mfma_f32_32x32x16_bf16(b0, qr[d0], d0 == 0 ? negm : p0, 0, 0, 0);
;         p1 = __builtin_amdgcn_mfma_f32_32x32x16_bf16(b1, qr[d0], d0 == 0 ? negm : p1, 0, 0, 0); }
.LBB4_944:
	v_exp_f32_e32 v182, v128
	v_exp_f32_e32 v234, v129
	v_exp_f32_e32 v235, v130
	v_exp_f32_e32 v236, v131
	v_exp_f32_e32 v237, v132
	v_exp_f32_e32 v238, v133
	v_exp_f32_e32 v239, v134
	v_exp_f32_e32 v240, v135
	v_exp_f32_e32 v241, v136
	v_exp_f32_e32 v242, v137
	v_exp_f32_e32 v243, v138
	v_exp_f32_e32 v244, v139
	v_exp_f32_e32 v245, v140
	v_exp_f32_e32 v246, v141
	v_exp_f32_e32 v247, v142
	v_exp_f32_e32 v248, v143
	v_add_u32_e32 v101, s54, v208
	v_add_u32_e32 v102, s54, v209
	v_add_u32_e32 v103, s54, v210
	ds_read_b128 v[172:175], v101 offset:49152
	ds_read_b128 v[176:179], v101 offset:53248
	ds_read_b128 v[218:221], v102 offset:49152
	ds_read_b128 v[222:225], v102 offset:53248
	ds_read_b128 v[226:229], v103 offset:49152
	ds_read_b128 v[230:233], v103 offset:53248
	v_exp_f32_e32 v112, v112
	v_exp_f32_e32 v113, v113
	v_exp_f32_e32 v114, v114
	s_waitcnt lgkmcnt(7)
	v_mfma_f32_32x32x16_bf16 v[128:143], v[96:99], v[156:159], v[80:95]
	v_exp_f32_e32 v115, v115
	v_exp_f32_e32 v116, v116
	v_exp_f32_e32 v117, v117
	v_exp_f32_e32 v118, v118
	v_exp_f32_e32 v119, v119
	s_waitcnt lgkmcnt(6)
	v_mfma_f32_32x32x16_bf16 v[96:111], v[168:171], v[156:159], v[80:95]
	v_exp_f32_e32 v168, v120
	v_add_f32_e32 v120, 0, v182
	v_add_f32_e32 v120, v234, v120
	v_add_f32_e32 v120, v235, v120
	v_add_f32_e32 v120, v236, v120
	v_add_f32_e32 v120, v237, v120
	v_add_f32_e32 v120, v238, v120
	v_add_f32_e32 v120, v239, v120
	v_add_f32_e32 v120, v240, v120
	v_add_f32_e32 v120, v241, v120
	v_add_f32_e32 v120, v242, v120
	s_waitcnt lgkmcnt(5)
	v_mfma_f32_32x32x16_bf16 v[128:143], v[172:175], v[152:155], v[128:143]
	v_add_f32_e32 v120, v243, v120
	v_add_f32_e32 v120, v244, v120
	v_add_f32_e32 v120, v245, v120
	v_add_f32_e32 v120, v246, v120
	v_add_f32_e32 v120, v247, v120
	v_add_f32_e32 v120, v248, v120
	v_add_f32_e32 v120, v112, v120
	s_waitcnt lgkmcnt(4)
	v_mfma_f32_32x32x16_bf16 v[96:111], v[176:179], v[152:155], v[96:111]
	v_add_f32_e32 v120, v113, v120
	v_add_f32_e32 v120, v114, v120
	v_add_f32_e32 v120, v115, v120
	v_add_f32_e32 v120, v116, v120
	v_exp_f32_e32 v169, v121
	v_add_f32_e32 v120, v117, v120
	v_exp_f32_e32 v170, v122
	s_waitcnt lgkmcnt(3)
	v_mfma_f32_32x32x16_bf16 v[128:143], v[218:221], v[148:151], v[128:143]
	v_add_f32_e32 v120, v118, v120
	v_exp_f32_e32 v171, v123
	v_add_f32_e32 v120, v119, v120
	v_exp_f32_e32 v172, v124
	v_add_f32_e32 v120, v168, v120
	v_exp_f32_e32 v173, v125
	v_add_f32_e32 v120, v169, v120
	s_waitcnt lgkmcnt(2)
	v_mfma_f32_32x32x16_bf16 v[96:111], v[222:225], v[148:151], v[96:111]
	v_exp_f32_e32 v174, v126
	v_add_f32_e32 v120, v170, v120
	v_exp_f32_e32 v175, v127
	v_add_f32_e32 v120, v171, v120
	v_add_f32_e32 v120, v172, v120
	v_add_f32_e32 v120, v173, v120
	v_add_f32_e32 v120, v174, v120
	s_waitcnt lgkmcnt(1)
	v_mfma_f32_32x32x16_bf16 v[128:143], v[226:229], v[144:147], v[128:143]
	v_add_f32_e32 v217, v175, v120
	v_mov_b32_e32 v218, v217
	v_cvt_pk_bf16_f32 v120, v182, v234
	v_cvt_pk_bf16_f32 v121, v235, v236
	v_cvt_pk_bf16_f32 v122, v237, v238
	v_cvt_pk_bf16_f32 v123, v239, v240
	v_cvt_pk_bf16_f32 v124, v241, v242
	s_waitcnt lgkmcnt(0)
	v_mfma_f32_32x32x16_bf16 v[96:111], v[230:233], v[144:147], v[96:111]
	v_cvt_pk_bf16_f32 v125, v243, v244
	v_cvt_pk_bf16_f32 v126, v245, v246
	v_cvt_pk_bf16_f32 v127, v247, v248
	v_cvt_pk_bf16_f32 v112, v112, v113
	v_cvt_pk_bf16_f32 v113, v114, v115
	v_cvt_pk_bf16_f32 v114, v116, v117
	v_cvt_pk_bf16_f32 v115, v118, v119
	v_cvt_pk_bf16_f32 v116, v168, v169
	v_cvt_pk_bf16_f32 v117, v170, v171
	v_cvt_pk_bf16_f32 v118, v172, v173
	v_cvt_pk_bf16_f32 v119, v174, v175
	v_permlane32_swap_b32_e32 v217, v218
	s_add_u32 s24, s34, 0x2380c000
	s_addc_u32 s25, s35, 0
	s_add_u32 s34, s34, 0x2380e000
	s_addc_u32 s35, s35, 0
	s_add_u32 s42, s42, 0x21886000
	s_addc_u32 s43, s43, 0
	global_load_dwordx4 v[176:179], v200, s[24:25]
	global_load_dwordx4 v[172:175], v200, s[34:35]
	s_nop 0
	global_load_dwordx4 v[168:171], v201, s[42:43]
	s_and_b64 vcc, exec, s[2:3]
	s_cbranch_vccnz .LBB4_946
	s_mov_b64 s[2:3], s[8:9]
	global_store_dwordx2 v193, v[184:185], s[2:3] nt

; #define AT_SBAR() __builtin_amdgcn_sched_barrier(0)
; template <int OFF> DI s16x4 tr_read(int vb) { s16x4 r; asm volatile("ds_read_b64_tr_b16 %0, %1 offset:%2" : "=&v"(r) : "v"(vb), "i"(OFF) : "memory"); return r; }
; template <int D0> DI void pv_one(f32x16& od, int vb, bf16x8 pa0, bf16x8 pa1, bf16x8 pa2, bf16x8 pa3) {
;     const s16x4 l0 = tr_read<v_rd_off(D0, 0, 0)>(vb), h0 = tr_read<v_rd_off(D0, 0, 1)>(vb), l1 = tr_read<v_rd_off(D0, 1, 0)>(vb), h1 = tr_read<v_rd_off(D0, 1, 1)>(vb);
;     const s16x4 l2 = tr_read<v_rd_off(D0, 2, 0)>(vb), h2 = tr_read<v_rd_off(D0, 2, 1)>(vb), l3 = tr_read<v_rd_off(D0, 3, 0)>(vb), h3 = tr_read<v_rd_off(D0, 3, 1)>(vb);
;     asm volatile("s_waitcnt lgkmcnt(0)" ::: "memory"); AT_SBAR();
;     ...
;     od = __builtin_amdgcn_mfma_f32_32x32x16_bf16(AT_PK(l0, h0), pa0, od, 0, 0, 0);
;     od = __builtin_amdgcn_mfma_f32_32x32x16_bf16(AT_PK(l1, h1), pa1, od, 0, 0, 0);
;     od = __builtin_amdgcn_mfma_f32_32x32x16_bf16(AT_PK(l2, h2), pa2, od, 0, 0, 0);
;     od = __builtin_amdgcn_mfma_f32_32x32x16_bf16(AT_PK(l3, h3), pa3, od, 0, 0, 0);
.LBB4_947:
	ds_read_b64_tr_b16 v[220:221], v219 offset:0x600
	ds_read_b64_tr_b16 v[222:223], v219 offset:0x700
	ds_read_b64_tr_b16 v[224:225], v219 offset:0x1600
	ds_read_b64_tr_b16 v[226:227], v219 offset:0x1700
	ds_read_b64_tr_b16 v[228:229], v219 offset:0x2600
	ds_read_b64_tr_b16 v[230:231], v219 offset:0x2700
	ds_read_b64_tr_b16 v[232:233], v219 offset:0x3600
	ds_read_b64_tr_b16 v[234:235], v219 offset:0x3700
	s_waitcnt lgkmcnt(0)
	s_nop 0
	v_mfma_f32_32x32x16_bf16 v[0:15], v[220:223], v[120:123], v[0:15]
	s_add_i32 s2, s31, 0
	v_add_u32_e32 v120, s2, v203
	s_waitcnt vmcnt(0)
	ds_write_b128 v120, v[176:179]
	s_mov_b32 s18, 0
	s_andn2_b64 vcc, exec, s[22:23]
	v_mfma_f32_32x32x16_bf16 v[0:15], v[224:227], v[124:127], v[0:15]
	v_mfma_f32_32x32x16_bf16 v[0:15], v[228:231], v[112:115], v[0:15]
	v_add_u32_e32 v112, s2, v204
	ds_write_b128 v112, v[172:175]
	v_lshl_add_u32 v112, s29, 13, v206
	ds_write_b128 v112, v[168:171] offset:49152
	s_andn2_b64 s[2:3], exec, s[22:23]
	v_mfma_f32_32x32x16_bf16 v[0:15], v[232:235], v[116:119], v[0:15]
	s_cbranch_vccnz .LBB4_952
	v_med3_f32 v113, v160, -v255, v255
	v_med3_f32 v114, v164, -v255, v255
	v_cvt_scalef32_pk_fp8_f32 v115, v113, v114, s93
	v_med3_f32 v113, v161, -v255, v255
	v_med3_f32 v114, v165, -v255, v255
	v_cvt_scalef32_pk_fp8_f32 v116, v113, v114, s93
	v_med3_f32 v113, v162, -v255, v255
	v_med3_f32 v114, v166, -v255, v255
	s_bitcmp1_b32 s58, 0
	v_cvt_scalef32_pk_fp8_f32 v117, v113, v114, s93
	s_cselect_b32 s8, 0x1100, 0
	v_med3_f32 v113, v163, -v255, v255
	v_med3_f32 v114, v167, -v255, v255
	v_cmp_eq_u32_e32 vcc, 0, v181
	v_add_u32_e32 v112, s8, v195
	v_cvt_scalef32_pk_fp8_f32 v118, v113, v114, s93
	s_and_b64 vcc, exec, vcc
	s_and_b32 s24, s58, 31
	ds_write_b16 v112, v115
	ds_write_b16 v112, v116 offset:68
	ds_write_b16 v112, v117 offset:136
	ds_write_b16 v112, v118 offset:204
	s_cbranch_vccnz .LBB4_957
	s_lshl_b32 s8, s24, 7
	s_lshl_b32 s9, s58, 6
	s_and_b32 s8, s8, 0xf00
	s_and_b32 s9, s9, 64
	s_or_b32 s18, s8, s9
	s_cbranch_execnz .LBB4_951
